# k_g3 + EpiResQ epilogues (out-proj fp8, dense-down bf16/fp8): second row-half residual loads hoisted ahead of the first half's stores (one round trip instead of two)
# baseline (speedup 1.0000x reference)
; __device__ __forceinline__ u32x4 pack8(const f32x4 a, const f32x4 b) { u32x4 w; w.x = cvt_pk_bf16(a[0], a[1]); w.y = cvt_pk_bf16(a[2], a[3]); w.z = cvt_pk_bf16(b[0], b[1]); w.w = cvt_pk_bf16(b[2], b[3]); return w; }
; __device__ __forceinline__ float sumsq4(const f32x4 v) { return (v[0] * v[0] + v[1] * v[1]) + (v[2] * v[2] + v[3] * v[3]); }
; __device__ __forceinline__ float xor16_add(float v) { return v + __int_as_float(__builtin_amdgcn_ds_swizzle(__float_as_int(v), 0x401F)); }
; __device__ __forceinline__ float xor32_add(float v) { auto rr = __builtin_amdgcn_permlane32_swap(__float_as_uint(v), __float_as_uint(v), false, false); return __uint_as_float(rr[0]) + __uint_as_float(rr[1]); }
; __device__ __forceinline__ f32x4 bf2f_lo(const u32x4 w, int h) { const unsigned a = h ? w.z : w.x, b = h ? w.w : w.y; return (f32x4){__uint_as_float(a << 16), __uint_as_float(a & 0xffff0000u), __uint_as_float(b << 16), __uint_as_float(b & 0xffff0000u)}; }
;     __device__ __forceinline__ void operator()(const f32x4 (&acc)[2][2][4][2], const Unit& u, int wr, int wc, int fr, int fq) const {
;     ...
;         const int row0 = u.pm * BM + wr * 64 + fr, col0 = u.pn * BM + wc * 32 + 8 * fq;
; #pragma unroll
;         for (int ai = 0; ai < 2; ++ai) {
;             u32x4 old[4][2];
; #pragma unroll
;             for (int m = 0; m < 4; ++m)
; #pragma unroll
;                 for (int bj = 0; bj < 2; ++bj) old[m][bj] = *(const u32x4*)(xb + (size_t)(row0 + ai * HALF + m * 16) * DM + col0 + bj * HALF);
; #pragma unroll
;             for (int m = 0; m < 4; ++m) {
;                 const int row = row0 + ai * HALF + m * 16; float ss = 0.f;
; #pragma unroll
;                 for (int bj = 0; bj < 2; ++bj) {
;                     const f32x4 v0 = bf2f_lo(old[m][bj], 0) + acc[ai][bj][m][0], v1 = bf2f_lo(old[m][bj], 1) + acc[ai][bj][m][1];
;                     ss += sumsq4(v0) + sumsq4(v1);
;                     *(u32x4*)(xb + (size_t)row * DM + col0 + bj * HALF) = pack8(v0, v1);
;                     { u32x2 w8; w8.x = pack4_fp8_x8(v0); w8.y = pack4_fp8_x8(v1); *(u32x2*)(xq + (size_t)row * DM + col0 + bj * HALF) = w8; }
;                 }
;                 ss = xor32_add(xor16_add(ss));
;                 if (fq == 0) ssx[(size_t)row * 16 + u.pn * 4 + wc] = ss;
.LBB0_1045:
	v_lshl_add_u32 v32, s59, 8, v163
	v_lshl_or_b32 v2, s58, 8, v193
	v_ashrrev_i32_e32 v3, 31, v2
	v_ashrrev_i32_e32 v33, 31, v32
	v_lshl_add_u64 v[174:175], v[2:3], 1, s[20:21]
	v_lshl_add_u64 v[30:31], s[22:23], 0, v[2:3]
	v_lshlrev_b64 v[2:3], 11, v[32:33]
	s_nop 15
	s_nop 15
	v_lshl_add_u64 v[190:191], v[174:175], 0, v[2:3]
	global_load_dwordx4 v[204:207], v[190:191], off
	global_load_dwordx4 v[26:29], v[190:191], off offset:256
	v_or_b32_e32 v184, 16, v32
	v_ashrrev_i32_e32 v185, 31, v184
	v_or_b32_e32 v180, 32, v32
	v_lshlrev_b64 v[2:3], 11, v[184:185]
	v_ashrrev_i32_e32 v181, 31, v180
	v_or_b32_e32 v176, 48, v32
	v_lshl_add_u64 v[186:187], v[174:175], 0, v[2:3]
	v_lshlrev_b64 v[2:3], 11, v[180:181]
	v_ashrrev_i32_e32 v177, 31, v176
	v_lshl_add_u64 v[182:183], v[174:175], 0, v[2:3]
	v_lshlrev_b64 v[2:3], 11, v[176:177]
	v_lshl_add_u64 v[178:179], v[174:175], 0, v[2:3]
	global_load_dwordx4 v[22:25], v[186:187], off
	global_load_dwordx4 v[18:21], v[186:187], off offset:256
	global_load_dwordx4 v[14:17], v[182:183], off
	global_load_dwordx4 v[10:13], v[182:183], off offset:256
	global_load_dwordx4 v[6:9], v[178:179], off
	global_load_dwordx4 v[2:5], v[178:179], off offset:256
	v_mov_b32_e32 v242, 0x40000
	v_mov_b32_e32 v243, 0
	v_lshl_add_u64 v[240:241], v[190:191], 0, v[242:243]
	global_load_dwordx4 v[208:211], v[240:241], off
	global_load_dwordx4 v[212:215], v[240:241], off offset:256
	v_lshl_add_u64 v[240:241], v[186:187], 0, v[242:243]
	global_load_dwordx4 v[216:219], v[240:241], off
	global_load_dwordx4 v[220:223], v[240:241], off offset:256
	v_lshl_add_u64 v[240:241], v[182:183], 0, v[242:243]
	global_load_dwordx4 v[224:227], v[240:241], off
	global_load_dwordx4 v[228:231], v[240:241], off offset:256
	v_lshl_add_u64 v[240:241], v[178:179], 0, v[242:243]
	global_load_dwordx4 v[232:235], v[240:241], off
	global_load_dwordx4 v[236:239], v[240:241], off offset:256
	v_lshlrev_b64 v[188:189], 10, v[32:33]
	v_lshl_add_u64 v[188:189], v[30:31], 0, v[188:189]
	s_lshl_b32 s24, s58, 2
	s_ashr_i32 s25, s24, 31
	s_lshl_b64 s[24:25], s[24:25], 2
	s_add_u32 s24, s49, s24
	s_addc_u32 s25, s50, s25
	s_waitcnt vmcnt(8)
	v_lshlrev_b32_e32 v196, 16, v204
	v_and_b32_e32 v197, 0xffff0000, v204
	v_lshlrev_b32_e32 v198, 16, v205
	v_and_b32_e32 v199, 0xffff0000, v205
	v_pk_add_f32 v[160:161], v[160:161], v[198:199]
	v_pk_add_f32 v[196:197], v[158:159], v[196:197]
	v_lshlrev_b32_e32 v158, 16, v206
	v_and_b32_e32 v159, 0xffff0000, v206
	v_lshlrev_b32_e32 v198, 16, v207
	v_and_b32_e32 v199, 0xffff0000, v207
	v_pk_add_f32 v[154:155], v[154:155], v[158:159]
	v_mul_f32_e32 v158, v197, v197
	v_mul_f32_e32 v159, v161, v161
	v_pk_add_f32 v[156:157], v[156:157], v[198:199]
	v_fmac_f32_e32 v158, v196, v196
	v_fmac_f32_e32 v159, v160, v160
	v_add_f32_e32 v158, v158, v159
	v_mul_f32_e32 v159, v155, v155
	v_mul_f32_e32 v195, v157, v157
	v_fmac_f32_e32 v159, v154, v154
	v_fmac_f32_e32 v195, v156, v156
	v_cvt_pk_bf16_f32 v204, v196, v197
	v_cvt_pk_bf16_f32 v205, v160, v161
	v_cvt_pk_bf16_f32 v206, v154, v155
	v_mul_f32_e32 v154, 0x41000000, v154
	v_mul_f32_e32 v155, 0x41000000, v155
	v_add_f32_e32 v159, v159, v195
	v_mul_f32_e32 v195, 0x41000000, v197
	v_med3_f32 v154, v154, s64, v250
	v_med3_f32 v155, v155, s64, v250
	v_mov_b32_e32 v197, v1
	v_cvt_pk_fp8_f32 v197, v154, v155
	v_add_f32_e32 v158, v158, v159
	v_mul_f32_e32 v159, 0x41000000, v196
	v_mul_f32_e32 v154, 0x41000000, v156
	v_mul_f32_e32 v155, 0x41000000, v157
	v_med3_f32 v159, v159, s64, v250
	v_med3_f32 v195, v195, s64, v250
	v_mov_b32_e32 v196, v1
	v_med3_f32 v154, v154, s64, v250
	v_med3_f32 v155, v155, s64, v250
	v_cvt_pk_fp8_f32 v196, v159, v195
	v_cvt_pk_fp8_f32 v197, v154, v155 op_sel:[0,0,1]
	v_lshlrev_b32_e32 v154, 16, v26
	v_and_b32_e32 v155, 0xffff0000, v26
	v_lshlrev_b32_e32 v26, 16, v27
	v_and_b32_e32 v27, 0xffff0000, v27
	v_pk_add_f32 v[26:27], v[152:153], v[26:27]
	v_pk_add_f32 v[150:151], v[150:151], v[154:155]
	v_lshlrev_b32_e32 v152, 16, v28
	v_and_b32_e32 v153, 0xffff0000, v28
	v_mul_f32_e32 v159, 0x41000000, v160
	v_mul_f32_e32 v160, 0x41000000, v161
	v_lshlrev_b32_e32 v28, 16, v29
	v_and_b32_e32 v29, 0xffff0000, v29
	v_pk_add_f32 v[152:153], v[146:147], v[152:153]
	v_mul_f32_e32 v146, v151, v151
	v_mul_f32_e32 v147, v27, v27
	v_med3_f32 v159, v159, s64, v250
	v_med3_f32 v160, v160, s64, v250
	v_pk_add_f32 v[28:29], v[148:149], v[28:29]
	v_fmac_f32_e32 v146, v150, v150
	v_fmac_f32_e32 v147, v26, v26
	v_cvt_pk_fp8_f32 v196, v159, v160 op_sel:[0,0,1]
	v_add_f32_e32 v146, v146, v147
	v_mul_f32_e32 v147, v153, v153
	v_mul_f32_e32 v148, v29, v29
	v_fmac_f32_e32 v147, v152, v152
	v_fmac_f32_e32 v148, v28, v28
	v_add_f32_e32 v147, v147, v148
	v_add_f32_e32 v146, v146, v147
	v_cvt_pk_bf16_f32 v207, v156, v157
	global_store_dwordx4 v[190:191], v[204:207], off
	global_store_dwordx2 v[188:189], v[196:197], off
	v_add_f32_e32 v154, v158, v146
	v_cvt_pk_bf16_f32 v146, v150, v151
	v_cvt_pk_bf16_f32 v147, v26, v27
	v_cvt_pk_bf16_f32 v148, v152, v153
	v_cvt_pk_bf16_f32 v149, v28, v29
	global_store_dwordx4 v[190:191], v[146:149], off offset:256
	v_mul_f32_e32 v26, 0x41000000, v26
	v_mul_f32_e32 v27, 0x41000000, v27
	v_mul_f32_e32 v146, 0x41000000, v150
	v_med3_f32 v147, v146, s64, v250
	v_mul_f32_e32 v146, 0x41000000, v151
	v_med3_f32 v148, v146, s64, v250
	v_mov_b32_e32 v146, v1
	v_cvt_pk_fp8_f32 v146, v147, v148
	v_med3_f32 v26, v26, s64, v250
	v_med3_f32 v27, v27, s64, v250
	v_mov_b32_e32 v147, v1
	v_cvt_pk_fp8_f32 v146, v26, v27 op_sel:[0,0,1]
	v_mul_f32_e32 v26, 0x41000000, v152
	v_mul_f32_e32 v27, 0x41000000, v153
	v_med3_f32 v26, v26, s64, v250
	v_med3_f32 v27, v27, s64, v250
	v_cvt_pk_fp8_f32 v147, v26, v27
	v_mul_f32_e32 v26, 0x41000000, v28
	v_mul_f32_e32 v27, 0x41000000, v29
	v_med3_f32 v26, v26, s64, v250
	v_med3_f32 v27, v27, s64, v250
	v_cvt_pk_fp8_f32 v147, v26, v27 op_sel:[0,0,1]
	ds_swizzle_b32 v26, v154 offset:swizzle(SWAP,16)
	global_store_dwordx2 v[188:189], v[146:147], off offset:128
	s_waitcnt lgkmcnt(0)
	v_add_f32_e32 v26, v154, v26
	v_mov_b32_e32 v27, v26
	s_nop 1
	v_permlane32_swap_b32_e32 v26, v27
	s_and_saveexec_b64 s[26:27], s[2:3]
	s_cbranch_execz .LBB0_1047
	v_lshlrev_b64 v[28:29], 6, v[32:33]
	v_lshl_add_u64 v[28:29], s[24:25], 0, v[28:29]
	v_add_f32_e32 v26, v26, v27
	global_store_dword v[28:29], v26, off

; __device__ __forceinline__ u32x4 pack8(const f32x4 a, const f32x4 b) { u32x4 w; w.x = cvt_pk_bf16(a[0], a[1]); w.y = cvt_pk_bf16(a[2], a[3]); w.z = cvt_pk_bf16(b[0], b[1]); w.w = cvt_pk_bf16(b[2], b[3]); return w; }
; __device__ __forceinline__ float sumsq4(const f32x4 v) { return (v[0] * v[0] + v[1] * v[1]) + (v[2] * v[2] + v[3] * v[3]); }
; __device__ __forceinline__ float xor16_add(float v) { return v + __int_as_float(__builtin_amdgcn_ds_swizzle(__float_as_int(v), 0x401F)); }
; __device__ __forceinline__ float xor32_add(float v) { auto rr = __builtin_amdgcn_permlane32_swap(__float_as_uint(v), __float_as_uint(v), false, false); return __uint_as_float(rr[0]) + __uint_as_float(rr[1]); }
; __device__ __forceinline__ f32x4 bf2f_lo(const u32x4 w, int h) { const unsigned a = h ? w.z : w.x, b = h ? w.w : w.y; return (f32x4){__uint_as_float(a << 16), __uint_as_float(a & 0xffff0000u), __uint_as_float(b << 16), __uint_as_float(b & 0xffff0000u)}; }
;     __device__ __forceinline__ void operator()(const f32x4 (&acc)[2][2][4][2], const Unit& u, int wr, int wc, int fr, int fq) const {
;     ...
;                 for (int bj = 0; bj < 2; ++bj) old[m][bj] = *(const u32x4*)(xb + (size_t)(row0 + ai * HALF + m * 16) * DM + col0 + bj * HALF);
; #pragma unroll
;             for (int m = 0; m < 4; ++m) {
;                 const int row = row0 + ai * HALF + m * 16; float ss = 0.f;
; #pragma unroll
;                 for (int bj = 0; bj < 2; ++bj) {
;                     const f32x4 v0 = bf2f_lo(old[m][bj], 0) + acc[ai][bj][m][0], v1 = bf2f_lo(old[m][bj], 1) + acc[ai][bj][m][1];
;                     ss += sumsq4(v0) + sumsq4(v1);
;                     *(u32x4*)(xb + (size_t)row * DM + col0 + bj * HALF) = pack8(v0, v1);
;                     { u32x2 w8; w8.x = pack4_fp8_x8(v0); w8.y = pack4_fp8_x8(v1); *(u32x2*)(xq + (size_t)row * DM + col0 + bj * HALF) = w8; }
;                 }
;                 ss = xor32_add(xor16_add(ss));
;                 if (fq == 0) ssx[(size_t)row * 16 + u.pn * 4 + wc] = ss;
.LBB0_1053:
	s_or_b64 exec, exec, s[26:27]
	v_add_u32_e32 v108, 0x80, v32
	v_ashrrev_i32_e32 v109, 31, v108
	v_lshlrev_b64 v[2:3], 11, v[108:109]
	v_lshl_add_u64 v[110:111], v[174:175], 0, v[2:3]
	v_add_u32_e32 v104, 0x90, v32
	v_ashrrev_i32_e32 v105, 31, v104
	v_add_u32_e32 v100, 0xa0, v32
	v_lshlrev_b64 v[2:3], 11, v[104:105]
	v_ashrrev_i32_e32 v101, 31, v100
	v_add_u32_e32 v32, 0xb0, v32
	v_lshl_add_u64 v[106:107], v[174:175], 0, v[2:3]
	v_lshlrev_b64 v[2:3], 11, v[100:101]
	v_ashrrev_i32_e32 v33, 31, v32
	v_lshl_add_u64 v[102:103], v[174:175], 0, v[2:3]
	v_lshlrev_b64 v[2:3], 11, v[32:33]
	v_lshl_add_u64 v[98:99], v[174:175], 0, v[2:3]
	s_waitcnt vmcnt(16)
	v_mov_b32_e32 v114, v208
	v_mov_b32_e32 v115, v209
	v_mov_b32_e32 v116, v210
	v_mov_b32_e32 v117, v211
	v_mov_b32_e32 v26, v212
	v_mov_b32_e32 v27, v213
	v_mov_b32_e32 v28, v214
	v_mov_b32_e32 v29, v215
	v_mov_b32_e32 v22, v216
	v_mov_b32_e32 v23, v217
	v_mov_b32_e32 v24, v218
	v_mov_b32_e32 v25, v219
	v_mov_b32_e32 v18, v220
	v_mov_b32_e32 v19, v221
	v_mov_b32_e32 v20, v222
	v_mov_b32_e32 v21, v223
	v_mov_b32_e32 v14, v224
	v_mov_b32_e32 v15, v225
	v_mov_b32_e32 v16, v226
	v_mov_b32_e32 v17, v227
	v_mov_b32_e32 v10, v228
	v_mov_b32_e32 v11, v229
	v_mov_b32_e32 v12, v230
	v_mov_b32_e32 v13, v231
	v_mov_b32_e32 v6, v232
	v_mov_b32_e32 v7, v233
	v_mov_b32_e32 v8, v234
	v_mov_b32_e32 v9, v235
	v_mov_b32_e32 v2, v236
	v_mov_b32_e32 v3, v237
	v_mov_b32_e32 v4, v238
	v_mov_b32_e32 v5, v239
	v_lshlrev_b64 v[112:113], 10, v[108:109]
	v_lshl_add_u64 v[112:113], v[30:31], 0, v[112:113]
	v_lshlrev_b32_e32 v118, 16, v114
	v_and_b32_e32 v119, 0xffff0000, v114
	v_lshlrev_b32_e32 v114, 16, v115
	v_and_b32_e32 v115, 0xffff0000, v115
	v_pk_add_f32 v[114:115], v[96:97], v[114:115]
	v_pk_add_f32 v[118:119], v[94:95], v[118:119]
	v_lshlrev_b32_e32 v94, 16, v116
	v_and_b32_e32 v95, 0xffff0000, v116
	v_lshlrev_b32_e32 v96, 16, v117
	v_and_b32_e32 v97, 0xffff0000, v117
	v_pk_add_f32 v[116:117], v[90:91], v[94:95]
	v_mul_f32_e32 v90, v119, v119
	v_mul_f32_e32 v91, v115, v115
	v_pk_add_f32 v[92:93], v[92:93], v[96:97]
	v_fmac_f32_e32 v90, v118, v118
	v_fmac_f32_e32 v91, v114, v114
	v_add_f32_e32 v90, v90, v91
	v_mul_f32_e32 v91, v117, v117
	v_mul_f32_e32 v94, v93, v93
	v_fmac_f32_e32 v91, v116, v116
	v_fmac_f32_e32 v94, v92, v92
	v_add_f32_e32 v91, v91, v94
	v_cvt_pk_bf16_f32 v94, v118, v119
	v_add_f32_e32 v90, v90, v91
	v_cvt_pk_bf16_f32 v95, v114, v115
	v_cvt_pk_bf16_f32 v96, v116, v117
	v_cvt_pk_bf16_f32 v97, v92, v93
	global_store_dwordx4 v[110:111], v[94:97], off
	v_mul_f32_e32 v91, 0x41000000, v118
	v_med3_f32 v91, v91, s64, v250
	v_mul_f32_e32 v94, 0x41000000, v119
	v_med3_f32 v95, v94, s64, v250
	v_mov_b32_e32 v94, v1
	v_cvt_pk_fp8_f32 v94, v91, v95
	v_mul_f32_e32 v91, 0x41000000, v114
	v_mul_f32_e32 v95, 0x41000000, v115
	v_med3_f32 v91, v91, s64, v250
	v_med3_f32 v95, v95, s64, v250
	v_cvt_pk_fp8_f32 v94, v91, v95 op_sel:[0,0,1]
	v_mul_f32_e32 v91, 0x41000000, v116
	v_mul_f32_e32 v95, 0x41000000, v117
	v_med3_f32 v91, v91, s64, v250
	v_med3_f32 v96, v95, s64, v250
	v_mov_b32_e32 v95, v1
	v_cvt_pk_fp8_f32 v95, v91, v96
	v_mul_f32_e32 v91, 0x41000000, v92
	v_mul_f32_e32 v92, 0x41000000, v93
	v_med3_f32 v91, v91, s64, v250
	v_med3_f32 v92, v92, s64, v250
	v_cvt_pk_fp8_f32 v95, v91, v92 op_sel:[0,0,1]
	v_lshlrev_b32_e32 v92, 16, v26
	v_and_b32_e32 v93, 0xffff0000, v26
	v_lshlrev_b32_e32 v26, 16, v27
	v_and_b32_e32 v27, 0xffff0000, v27
	v_pk_add_f32 v[26:27], v[88:89], v[26:27]
	v_pk_add_f32 v[86:87], v[86:87], v[92:93]
	v_lshlrev_b32_e32 v88, 16, v28
	v_and_b32_e32 v89, 0xffff0000, v28
	v_lshlrev_b32_e32 v28, 16, v29
	v_and_b32_e32 v29, 0xffff0000, v29
	v_pk_add_f32 v[88:89], v[82:83], v[88:89]
	v_mul_f32_e32 v82, v87, v87
	v_mul_f32_e32 v83, v27, v27
	v_pk_add_f32 v[28:29], v[84:85], v[28:29]
	v_fmac_f32_e32 v82, v86, v86
	v_fmac_f32_e32 v83, v26, v26
	v_add_f32_e32 v82, v82, v83
	v_mul_f32_e32 v83, v89, v89
	v_mul_f32_e32 v84, v29, v29
	v_fmac_f32_e32 v83, v88, v88
	v_fmac_f32_e32 v84, v28, v28
	v_add_f32_e32 v83, v83, v84
	v_add_f32_e32 v82, v82, v83
	global_store_dwordx2 v[112:113], v[94:95], off
	v_add_f32_e32 v90, v90, v82
	v_cvt_pk_bf16_f32 v82, v86, v87
	v_cvt_pk_bf16_f32 v83, v26, v27
	v_cvt_pk_bf16_f32 v84, v88, v89
	v_cvt_pk_bf16_f32 v85, v28, v29
	global_store_dwordx4 v[110:111], v[82:85], off offset:256
	v_mul_f32_e32 v26, 0x41000000, v26
	v_mul_f32_e32 v27, 0x41000000, v27
	v_mul_f32_e32 v82, 0x41000000, v86
	v_med3_f32 v83, v82, s64, v250
	v_mul_f32_e32 v82, 0x41000000, v87
	v_med3_f32 v84, v82, s64, v250
	v_mov_b32_e32 v82, v1
	v_cvt_pk_fp8_f32 v82, v83, v84
	v_med3_f32 v26, v26, s64, v250
	v_med3_f32 v27, v27, s64, v250
	v_mov_b32_e32 v83, v1
	v_cvt_pk_fp8_f32 v82, v26, v27 op_sel:[0,0,1]
	v_mul_f32_e32 v26, 0x41000000, v88
	v_mul_f32_e32 v27, 0x41000000, v89
	v_med3_f32 v26, v26, s64, v250
	v_med3_f32 v27, v27, s64, v250
	v_cvt_pk_fp8_f32 v83, v26, v27
	v_mul_f32_e32 v26, 0x41000000, v28
	v_mul_f32_e32 v27, 0x41000000, v29
	v_med3_f32 v26, v26, s64, v250
	v_med3_f32 v27, v27, s64, v250
	v_cvt_pk_fp8_f32 v83, v26, v27 op_sel:[0,0,1]
	ds_swizzle_b32 v26, v90 offset:swizzle(SWAP,16)
	global_store_dwordx2 v[112:113], v[82:83], off offset:128
	s_waitcnt lgkmcnt(0)
	v_add_f32_e32 v26, v90, v26
	v_mov_b32_e32 v27, v26
	s_nop 1
	v_permlane32_swap_b32_e32 v26, v27
	s_and_saveexec_b64 s[26:27], s[2:3]
	s_cbranch_execz .LBB0_1055
	v_lshlrev_b64 v[28:29], 6, v[108:109]
	v_lshl_add_u64 v[28:29], s[24:25], 0, v[28:29]
	v_add_f32_e32 v26, v26, v27
	global_store_dword v[28:29], v26, off
; __device__ __forceinline__ u32x4 pack8(const f32x4 a, const f32x4 b) { u32x4 w; w.x = cvt_pk_bf16(a[0], a[1]); w.y = cvt_pk_bf16(a[2], a[3]); w.z = cvt_pk_bf16(b[0], b[1]); w.w = cvt_pk_bf16(b[2], b[3]); return w; }
; __device__ __forceinline__ float sumsq4(const f32x4 v) { return (v[0] * v[0] + v[1] * v[1]) + (v[2] * v[2] + v[3] * v[3]); }
; __device__ __forceinline__ float xor16_add(float v) { return v + __int_as_float(__builtin_amdgcn_ds_swizzle(__float_as_int(v), 0x401F)); }
; __device__ __forceinline__ float xor32_add(float v) { auto rr = __builtin_amdgcn_permlane32_swap(__float_as_uint(v), __float_as_uint(v), false, false); return __uint_as_float(rr[0]) + __uint_as_float(rr[1]); }
; __device__ __forceinline__ f32x4 bf2f_lo(const u32x4 w, int h) { const unsigned a = h ? w.z : w.x, b = h ? w.w : w.y; return (f32x4){__uint_as_float(a << 16), __uint_as_float(a & 0xffff0000u), __uint_as_float(b << 16), __uint_as_float(b & 0xffff0000u)}; }
;     __device__ __forceinline__ void operator()(const f32x4 (&acc)[2][2][4][2], const Unit& u, int wr, int wc, int fr, int fq) const {
;     ...
;             for (int m = 0; m < 4; ++m) {
;                 const int row = row0 + ai * HALF + m * 16; float ss = 0.f;
; #pragma unroll
;                 for (int bj = 0; bj < 2; ++bj) {
;                     const f32x4 v0 = bf2f_lo(old[m][bj], 0) + acc[ai][bj][m][0], v1 = bf2f_lo(old[m][bj], 1) + acc[ai][bj][m][1];
;                     ss += sumsq4(v0) + sumsq4(v1);
;                     *(u32x4*)(xb + (size_t)row * DM + col0 + bj * HALF) = pack8(v0, v1);
;                     { u32x2 w8; w8.x = pack4_fp8_x8(v0); w8.y = pack4_fp8_x8(v1); *(u32x2*)(xq + (size_t)row * DM + col0 + bj * HALF) = w8; }
;                 }
;                 ss = xor32_add(xor16_add(ss));
;                 if (fq == 0) ssx[(size_t)row * 16 + u.pn * 4 + wc] = ss;
.LBB0_1055:
	s_or_b64 exec, exec, s[26:27]
	v_lshlrev_b32_e32 v28, 16, v22
	v_and_b32_e32 v29, 0xffff0000, v22
	v_lshlrev_b32_e32 v22, 16, v23
	v_and_b32_e32 v23, 0xffff0000, v23
	v_pk_add_f32 v[80:81], v[80:81], v[22:23]
	v_pk_add_f32 v[28:29], v[78:79], v[28:29]
	v_lshlrev_b32_e32 v22, 16, v24
	v_and_b32_e32 v23, 0xffff0000, v24
	v_lshlrev_b32_e32 v24, 16, v25
	v_and_b32_e32 v25, 0xffff0000, v25
	v_pk_add_f32 v[76:77], v[76:77], v[24:25]
	v_pk_add_f32 v[24:25], v[74:75], v[22:23]
	v_mul_f32_e32 v22, v29, v29
	v_mul_f32_e32 v23, v81, v81
	v_fmac_f32_e32 v22, v28, v28
	v_fmac_f32_e32 v23, v80, v80
	v_add_f32_e32 v22, v22, v23
	v_mul_f32_e32 v23, v25, v25
	v_mul_f32_e32 v74, v77, v77
	v_fmac_f32_e32 v23, v24, v24
	v_fmac_f32_e32 v74, v76, v76
	v_add_f32_e32 v23, v23, v74
	v_add_f32_e32 v74, v22, v23
	v_cvt_pk_bf16_f32 v22, v28, v29
	v_mul_f32_e32 v28, 0x41000000, v28
	v_med3_f32 v75, v28, s64, v250
	v_mul_f32_e32 v28, 0x41000000, v29
	v_med3_f32 v29, v28, s64, v250
	v_mov_b32_e32 v28, v1
	v_cvt_pk_fp8_f32 v28, v75, v29
	v_mul_f32_e32 v29, 0x41000000, v80
	v_mul_f32_e32 v75, 0x41000000, v81
	v_med3_f32 v29, v29, s64, v250
	v_med3_f32 v75, v75, s64, v250
	v_cvt_pk_fp8_f32 v28, v29, v75 op_sel:[0,0,1]
	v_mul_f32_e32 v29, 0x41000000, v24
	v_med3_f32 v75, v29, s64, v250
	v_mul_f32_e32 v29, 0x41000000, v25
	v_med3_f32 v78, v29, s64, v250
	v_mov_b32_e32 v29, v1
	v_cvt_pk_fp8_f32 v29, v75, v78
	v_mul_f32_e32 v75, 0x41000000, v76
	v_mul_f32_e32 v78, 0x41000000, v77
	v_med3_f32 v75, v75, s64, v250
	v_med3_f32 v78, v78, s64, v250
	v_cvt_pk_fp8_f32 v29, v75, v78 op_sel:[0,0,1]
	v_lshlrev_b64 v[26:27], 10, v[104:105]
	v_cvt_pk_bf16_f32 v23, v80, v81
	v_cvt_pk_bf16_f32 v24, v24, v25
	v_cvt_pk_bf16_f32 v25, v76, v77
	v_lshl_add_u64 v[26:27], v[30:31], 0, v[26:27]
	global_store_dwordx4 v[106:107], v[22:25], off
	global_store_dwordx2 v[26:27], v[28:29], off
	v_lshlrev_b32_e32 v22, 16, v18
	v_and_b32_e32 v23, 0xffff0000, v18
	v_lshlrev_b32_e32 v18, 16, v19
	v_and_b32_e32 v19, 0xffff0000, v19
	v_pk_add_f32 v[24:25], v[72:73], v[18:19]
	v_pk_add_f32 v[22:23], v[70:71], v[22:23]
	v_lshlrev_b32_e32 v18, 16, v20
	v_and_b32_e32 v19, 0xffff0000, v20
	v_lshlrev_b32_e32 v20, 16, v21
	v_and_b32_e32 v21, 0xffff0000, v21
	v_pk_add_f32 v[28:29], v[68:69], v[20:21]
	v_pk_add_f32 v[20:21], v[66:67], v[18:19]
	v_mul_f32_e32 v18, v23, v23
	v_mul_f32_e32 v19, v25, v25
	v_fmac_f32_e32 v18, v22, v22
	v_fmac_f32_e32 v19, v24, v24
	v_add_f32_e32 v18, v18, v19
	v_mul_f32_e32 v19, v21, v21
	v_mul_f32_e32 v66, v29, v29
	v_fmac_f32_e32 v19, v20, v20
	v_fmac_f32_e32 v66, v28, v28
	v_add_f32_e32 v19, v19, v66
	v_add_f32_e32 v18, v18, v19
	v_add_f32_e32 v66, v74, v18
	v_cvt_pk_bf16_f32 v18, v22, v23
	v_mul_f32_e32 v22, 0x41000000, v22
	v_med3_f32 v67, v22, s64, v250
	v_mul_f32_e32 v22, 0x41000000, v23
	v_med3_f32 v23, v22, s64, v250
	v_mov_b32_e32 v22, v1
	v_cvt_pk_fp8_f32 v22, v67, v23
	v_cvt_pk_bf16_f32 v19, v24, v25
	v_mul_f32_e32 v23, 0x41000000, v24
	v_mul_f32_e32 v24, 0x41000000, v25
	v_med3_f32 v23, v23, s64, v250
	v_med3_f32 v24, v24, s64, v250
	v_cvt_pk_fp8_f32 v22, v23, v24 op_sel:[0,0,1]
	v_mul_f32_e32 v23, 0x41000000, v20
	v_med3_f32 v24, v23, s64, v250
	v_mul_f32_e32 v23, 0x41000000, v21
	v_med3_f32 v25, v23, s64, v250
	v_mov_b32_e32 v23, v1
	v_cvt_pk_fp8_f32 v23, v24, v25
	v_mul_f32_e32 v24, 0x41000000, v28
	v_mul_f32_e32 v25, 0x41000000, v29
	v_med3_f32 v24, v24, s64, v250
	v_med3_f32 v25, v25, s64, v250
	v_cvt_pk_fp8_f32 v23, v24, v25 op_sel:[0,0,1]
	ds_swizzle_b32 v24, v66 offset:swizzle(SWAP,16)
	v_cvt_pk_bf16_f32 v20, v20, v21
	v_cvt_pk_bf16_f32 v21, v28, v29
	global_store_dwordx4 v[106:107], v[18:21], off offset:256
	global_store_dwordx2 v[26:27], v[22:23], off offset:128
	s_waitcnt lgkmcnt(0)
	v_add_f32_e32 v18, v66, v24
	v_mov_b32_e32 v19, v18
	s_nop 1
	v_permlane32_swap_b32_e32 v18, v19
	s_and_saveexec_b64 s[26:27], s[2:3]
	s_cbranch_execz .LBB0_1057
	v_lshlrev_b64 v[20:21], 6, v[104:105]
	v_lshl_add_u64 v[20:21], s[24:25], 0, v[20:21]
	v_add_f32_e32 v18, v18, v19
	global_store_dword v[20:21], v18, off
.LBB0_1057:
	s_or_b64 exec, exec, s[26:27]
	v_lshlrev_b32_e32 v20, 16, v14
	v_and_b32_e32 v21, 0xffff0000, v14
	v_lshlrev_b32_e32 v14, 16, v15
	v_and_b32_e32 v15, 0xffff0000, v15
	v_pk_add_f32 v[22:23], v[64:65], v[14:15]
	v_pk_add_f32 v[20:21], v[62:63], v[20:21]
	v_lshlrev_b32_e32 v14, 16, v16
	v_and_b32_e32 v15, 0xffff0000, v16
	v_lshlrev_b32_e32 v16, 16, v17
	v_and_b32_e32 v17, 0xffff0000, v17
	v_pk_add_f32 v[24:25], v[60:61], v[16:17]
	v_pk_add_f32 v[16:17], v[58:59], v[14:15]
	v_mul_f32_e32 v14, v21, v21
	v_mul_f32_e32 v15, v23, v23
	v_fmac_f32_e32 v14, v20, v20
	v_fmac_f32_e32 v15, v22, v22
	v_add_f32_e32 v14, v14, v15
	v_mul_f32_e32 v15, v17, v17
	v_mul_f32_e32 v26, v25, v25
	v_fmac_f32_e32 v15, v16, v16
	v_fmac_f32_e32 v26, v24, v24
	v_add_f32_e32 v15, v15, v26
	v_add_f32_e32 v26, v14, v15
	v_cvt_pk_bf16_f32 v14, v20, v21
	v_mul_f32_e32 v20, 0x41000000, v20
	v_med3_f32 v27, v20, s64, v250
	v_mul_f32_e32 v20, 0x41000000, v21
	v_med3_f32 v21, v20, s64, v250
	v_mov_b32_e32 v20, v1
	v_cvt_pk_fp8_f32 v20, v27, v21
	v_cvt_pk_bf16_f32 v15, v22, v23
	v_mul_f32_e32 v21, 0x41000000, v22
	v_mul_f32_e32 v22, 0x41000000, v23
	v_med3_f32 v21, v21, s64, v250
	v_med3_f32 v22, v22, s64, v250
	v_cvt_pk_fp8_f32 v20, v21, v22 op_sel:[0,0,1]
	v_mul_f32_e32 v21, 0x41000000, v16
	v_med3_f32 v22, v21, s64, v250
	v_mul_f32_e32 v21, 0x41000000, v17
	v_med3_f32 v23, v21, s64, v250
	v_mov_b32_e32 v21, v1
	v_cvt_pk_fp8_f32 v21, v22, v23
	v_mul_f32_e32 v22, 0x41000000, v24
	v_mul_f32_e32 v23, 0x41000000, v25
	v_med3_f32 v22, v22, s64, v250
	v_med3_f32 v23, v23, s64, v250
; __device__ __forceinline__ u32x4 pack8(const f32x4 a, const f32x4 b) { u32x4 w; w.x = cvt_pk_bf16(a[0], a[1]); w.y = cvt_pk_bf16(a[2], a[3]); w.z = cvt_pk_bf16(b[0], b[1]); w.w = cvt_pk_bf16(b[2], b[3]); return w; }
; __device__ __forceinline__ float sumsq4(const f32x4 v) { return (v[0] * v[0] + v[1] * v[1]) + (v[2] * v[2] + v[3] * v[3]); }
; __device__ __forceinline__ float xor16_add(float v) { return v + __int_as_float(__builtin_amdgcn_ds_swizzle(__float_as_int(v), 0x401F)); }
; __device__ __forceinline__ float xor32_add(float v) { auto rr = __builtin_amdgcn_permlane32_swap(__float_as_uint(v), __float_as_uint(v), false, false); return __uint_as_float(rr[0]) + __uint_as_float(rr[1]); }
; __device__ __forceinline__ f32x4 bf2f_lo(const u32x4 w, int h) { const unsigned a = h ? w.z : w.x, b = h ? w.w : w.y; return (f32x4){__uint_as_float(a << 16), __uint_as_float(a & 0xffff0000u), __uint_as_float(b << 16), __uint_as_float(b & 0xffff0000u)}; }
;     __device__ __forceinline__ void operator()(const f32x4 (&acc)[2][2][4][2], const Unit& u, int wr, int wc, int fr, int fq) const {
;     ...
;             for (int m = 0; m < 4; ++m) {
;                 const int row = row0 + ai * HALF + m * 16; float ss = 0.f;
; #pragma unroll
;                 for (int bj = 0; bj < 2; ++bj) {
;                     const f32x4 v0 = bf2f_lo(old[m][bj], 0) + acc[ai][bj][m][0], v1 = bf2f_lo(old[m][bj], 1) + acc[ai][bj][m][1];
;                     ss += sumsq4(v0) + sumsq4(v1);
;                     *(u32x4*)(xb + (size_t)row * DM + col0 + bj * HALF) = pack8(v0, v1);
;                     { u32x2 w8; w8.x = pack4_fp8_x8(v0); w8.y = pack4_fp8_x8(v1); *(u32x2*)(xq + (size_t)row * DM + col0 + bj * HALF) = w8; }
;                 }
;                 ss = xor32_add(xor16_add(ss));
;                 if (fq == 0) ssx[(size_t)row * 16 + u.pn * 4 + wc] = ss;
	v_cvt_pk_fp8_f32 v21, v22, v23 op_sel:[0,0,1]
	v_lshlrev_b64 v[18:19], 10, v[100:101]
	v_cvt_pk_bf16_f32 v16, v16, v17
	v_cvt_pk_bf16_f32 v17, v24, v25
	v_lshl_add_u64 v[18:19], v[30:31], 0, v[18:19]
	global_store_dwordx4 v[102:103], v[14:17], off
	global_store_dwordx2 v[18:19], v[20:21], off
	v_lshlrev_b32_e32 v14, 16, v10
	v_and_b32_e32 v15, 0xffff0000, v10
	v_lshlrev_b32_e32 v10, 16, v11
	v_and_b32_e32 v11, 0xffff0000, v11
	v_pk_add_f32 v[16:17], v[56:57], v[10:11]
	v_pk_add_f32 v[14:15], v[54:55], v[14:15]
	v_lshlrev_b32_e32 v10, 16, v12
	v_and_b32_e32 v11, 0xffff0000, v12
	v_lshlrev_b32_e32 v12, 16, v13
	v_and_b32_e32 v13, 0xffff0000, v13
	v_pk_add_f32 v[20:21], v[52:53], v[12:13]
	v_pk_add_f32 v[12:13], v[50:51], v[10:11]
	v_mul_f32_e32 v10, v15, v15
	v_mul_f32_e32 v11, v17, v17
	v_fmac_f32_e32 v10, v14, v14
	v_fmac_f32_e32 v11, v16, v16
	v_add_f32_e32 v10, v10, v11
	v_mul_f32_e32 v11, v13, v13
	v_mul_f32_e32 v22, v21, v21
	v_fmac_f32_e32 v11, v12, v12
	v_fmac_f32_e32 v22, v20, v20
	v_add_f32_e32 v11, v11, v22
	v_add_f32_e32 v10, v10, v11
	v_add_f32_e32 v22, v26, v10
	v_cvt_pk_bf16_f32 v10, v14, v15
	v_mul_f32_e32 v14, 0x41000000, v14
	v_med3_f32 v23, v14, s64, v250
	v_mul_f32_e32 v14, 0x41000000, v15
	v_med3_f32 v15, v14, s64, v250
	v_mov_b32_e32 v14, v1
	v_cvt_pk_fp8_f32 v14, v23, v15
	v_cvt_pk_bf16_f32 v11, v16, v17
	v_mul_f32_e32 v15, 0x41000000, v16
	v_mul_f32_e32 v16, 0x41000000, v17
	v_med3_f32 v15, v15, s64, v250
	v_med3_f32 v16, v16, s64, v250
	v_cvt_pk_fp8_f32 v14, v15, v16 op_sel:[0,0,1]
	v_mul_f32_e32 v15, 0x41000000, v12
	v_med3_f32 v16, v15, s64, v250
	v_mul_f32_e32 v15, 0x41000000, v13
	v_med3_f32 v17, v15, s64, v250
	v_mov_b32_e32 v15, v1
	v_cvt_pk_fp8_f32 v15, v16, v17
	v_mul_f32_e32 v16, 0x41000000, v20
	v_mul_f32_e32 v17, 0x41000000, v21
	v_med3_f32 v16, v16, s64, v250
	v_med3_f32 v17, v17, s64, v250
	v_cvt_pk_fp8_f32 v15, v16, v17 op_sel:[0,0,1]
	ds_swizzle_b32 v16, v22 offset:swizzle(SWAP,16)
	v_cvt_pk_bf16_f32 v12, v12, v13
	v_cvt_pk_bf16_f32 v13, v20, v21
	global_store_dwordx4 v[102:103], v[10:13], off offset:256
	global_store_dwordx2 v[18:19], v[14:15], off offset:128
	s_waitcnt lgkmcnt(0)
	v_add_f32_e32 v10, v22, v16
	v_mov_b32_e32 v11, v10
	s_nop 1
	v_permlane32_swap_b32_e32 v10, v11
	s_and_saveexec_b64 s[26:27], s[2:3]
	s_cbranch_execz .LBB0_1059
	v_lshlrev_b64 v[12:13], 6, v[100:101]
	v_lshl_add_u64 v[12:13], s[24:25], 0, v[12:13]
	v_add_f32_e32 v10, v10, v11
	global_store_dword v[12:13], v10, off
.LBB0_1059:
	s_or_b64 exec, exec, s[26:27]
	v_lshlrev_b32_e32 v12, 16, v6
	v_and_b32_e32 v13, 0xffff0000, v6
	v_lshlrev_b32_e32 v6, 16, v7
	v_and_b32_e32 v7, 0xffff0000, v7
	v_pk_add_f32 v[14:15], v[48:49], v[6:7]
	v_pk_add_f32 v[12:13], v[46:47], v[12:13]
	v_lshlrev_b32_e32 v6, 16, v8
	v_and_b32_e32 v7, 0xffff0000, v8
	v_lshlrev_b32_e32 v8, 16, v9
	v_and_b32_e32 v9, 0xffff0000, v9
	v_pk_add_f32 v[16:17], v[44:45], v[8:9]
	v_pk_add_f32 v[8:9], v[42:43], v[6:7]
	v_mul_f32_e32 v6, v13, v13
	v_mul_f32_e32 v7, v15, v15
	v_fmac_f32_e32 v6, v12, v12
	v_fmac_f32_e32 v7, v14, v14
	v_add_f32_e32 v6, v6, v7
	v_mul_f32_e32 v7, v9, v9
	v_mul_f32_e32 v18, v17, v17
	v_fmac_f32_e32 v7, v8, v8
	v_fmac_f32_e32 v18, v16, v16
	v_add_f32_e32 v7, v7, v18
	v_add_f32_e32 v18, v6, v7
	v_cvt_pk_bf16_f32 v6, v12, v13
	v_mul_f32_e32 v12, 0x41000000, v12
	v_med3_f32 v19, v12, s64, v250
	v_mul_f32_e32 v12, 0x41000000, v13
	v_med3_f32 v13, v12, s64, v250
	v_mov_b32_e32 v12, v1
	v_cvt_pk_fp8_f32 v12, v19, v13
	v_cvt_pk_bf16_f32 v7, v14, v15
	v_mul_f32_e32 v13, 0x41000000, v14
	v_mul_f32_e32 v14, 0x41000000, v15
	v_med3_f32 v13, v13, s64, v250
	v_med3_f32 v14, v14, s64, v250
	v_cvt_pk_fp8_f32 v12, v13, v14 op_sel:[0,0,1]
	v_mul_f32_e32 v13, 0x41000000, v8
	v_med3_f32 v14, v13, s64, v250
	v_mul_f32_e32 v13, 0x41000000, v9
	v_med3_f32 v15, v13, s64, v250
	v_mov_b32_e32 v13, v1
	v_cvt_pk_fp8_f32 v13, v14, v15
	v_mul_f32_e32 v14, 0x41000000, v16
	v_mul_f32_e32 v15, 0x41000000, v17
	v_med3_f32 v14, v14, s64, v250
	v_med3_f32 v15, v15, s64, v250
	v_cvt_pk_fp8_f32 v13, v14, v15 op_sel:[0,0,1]
	v_lshlrev_b64 v[10:11], 10, v[32:33]
	v_cvt_pk_bf16_f32 v8, v8, v9
	v_cvt_pk_bf16_f32 v9, v16, v17
	v_lshl_add_u64 v[10:11], v[30:31], 0, v[10:11]
	global_store_dwordx4 v[98:99], v[6:9], off
	global_store_dwordx2 v[10:11], v[12:13], off
	v_lshlrev_b32_e32 v6, 16, v2
	v_and_b32_e32 v7, 0xffff0000, v2
	v_lshlrev_b32_e32 v2, 16, v3
	v_and_b32_e32 v3, 0xffff0000, v3
	v_pk_add_f32 v[8:9], v[40:41], v[2:3]
	v_pk_add_f32 v[6:7], v[38:39], v[6:7]
	v_lshlrev_b32_e32 v2, 16, v4
	v_and_b32_e32 v3, 0xffff0000, v4
	v_lshlrev_b32_e32 v4, 16, v5
	v_and_b32_e32 v5, 0xffff0000, v5
	v_pk_add_f32 v[12:13], v[36:37], v[4:5]
	v_pk_add_f32 v[4:5], v[34:35], v[2:3]
	v_mul_f32_e32 v2, v7, v7
	v_mul_f32_e32 v3, v9, v9
	v_fmac_f32_e32 v2, v6, v6
	v_fmac_f32_e32 v3, v8, v8
	v_add_f32_e32 v2, v2, v3
	v_mul_f32_e32 v3, v5, v5
	v_mul_f32_e32 v14, v13, v13
	v_fmac_f32_e32 v3, v4, v4
	v_fmac_f32_e32 v14, v12, v12
	v_add_f32_e32 v3, v3, v14
	v_add_f32_e32 v2, v2, v3
	v_add_f32_e32 v14, v18, v2
	v_cvt_pk_bf16_f32 v2, v6, v7
	v_mul_f32_e32 v6, 0x41000000, v6
	v_med3_f32 v15, v6, s64, v250
	v_mul_f32_e32 v6, 0x41000000, v7
	v_med3_f32 v7, v6, s64, v250
	v_mov_b32_e32 v6, v1
	v_cvt_pk_fp8_f32 v6, v15, v7
	v_cvt_pk_bf16_f32 v3, v8, v9
	v_mul_f32_e32 v7, 0x41000000, v8
	v_mul_f32_e32 v8, 0x41000000, v9
	v_med3_f32 v7, v7, s64, v250
	v_med3_f32 v8, v8, s64, v250
	v_cvt_pk_fp8_f32 v6, v7, v8 op_sel:[0,0,1]
	v_mul_f32_e32 v7, 0x41000000, v4
	v_med3_f32 v8, v7, s64, v250
	v_mul_f32_e32 v7, 0x41000000, v5
	v_med3_f32 v9, v7, s64, v250
	v_mov_b32_e32 v7, v1
	v_cvt_pk_fp8_f32 v7, v8, v9
	v_mul_f32_e32 v8, 0x41000000, v12
	v_mul_f32_e32 v9, 0x41000000, v13
	v_med3_f32 v8, v8, s64, v250
	v_med3_f32 v9, v9, s64, v250
	v_cvt_pk_fp8_f32 v7, v8, v9 op_sel:[0,0,1]
	ds_swizzle_b32 v8, v14 offset:swizzle(SWAP,16)
	v_cvt_pk_bf16_f32 v4, v4, v5
	v_cvt_pk_bf16_f32 v5, v12, v13
	global_store_dwordx4 v[98:99], v[2:5], off offset:256
	global_store_dwordx2 v[10:11], v[6:7], off offset:128
	s_waitcnt lgkmcnt(0)
	v_add_f32_e32 v2, v14, v8
	v_mov_b32_e32 v3, v2
	s_nop 1
	v_permlane32_swap_b32_e32 v2, v3
	s_and_saveexec_b64 s[26:27], s[2:3]
	s_cbranch_execz .LBB0_1061
	v_lshlrev_b64 v[4:5], 6, v[32:33]
	v_lshl_add_u64 v[4:5], s[24:25], 0, v[4:5]
	v_add_f32_e32 v2, v2, v3
	global_store_dword v[4:5], v2, off

; __device__ __forceinline__ u32x4 pack8(const f32x4 a, const f32x4 b) { u32x4 w; w.x = cvt_pk_bf16(a[0], a[1]); w.y = cvt_pk_bf16(a[2], a[3]); w.z = cvt_pk_bf16(b[0], b[1]); w.w = cvt_pk_bf16(b[2], b[3]); return w; }
; __device__ __forceinline__ float sumsq4(const f32x4 v) { return (v[0] * v[0] + v[1] * v[1]) + (v[2] * v[2] + v[3] * v[3]); }
; __device__ __forceinline__ float xor16_add(float v) { return v + __int_as_float(__builtin_amdgcn_ds_swizzle(__float_as_int(v), 0x401F)); }
; __device__ __forceinline__ float xor32_add(float v) { auto rr = __builtin_amdgcn_permlane32_swap(__float_as_uint(v), __float_as_uint(v), false, false); return __uint_as_float(rr[0]) + __uint_as_float(rr[1]); }
; __device__ __forceinline__ f32x4 bf2f_lo(const u32x4 w, int h) { const unsigned a = h ? w.z : w.x, b = h ? w.w : w.y; return (f32x4){__uint_as_float(a << 16), __uint_as_float(a & 0xffff0000u), __uint_as_float(b << 16), __uint_as_float(b & 0xffff0000u)}; }
;     __device__ __forceinline__ void operator()(const f32x4 (&acc)[2][2][4][2], const Unit& u, int wr, int wc, int fr, int fq) const {
;     ...
;         const int row0 = u.pm * BM + wr * 64 + fr, col0 = u.pn * BM + wc * 32 + 8 * fq;
; #pragma unroll
;         for (int ai = 0; ai < 2; ++ai) {
;             u32x4 old[4][2];
; #pragma unroll
;             for (int m = 0; m < 4; ++m)
; #pragma unroll
;                 for (int bj = 0; bj < 2; ++bj) old[m][bj] = *(const u32x4*)(xb + (size_t)(row0 + ai * HALF + m * 16) * DM + col0 + bj * HALF);
; #pragma unroll
;             for (int m = 0; m < 4; ++m) {
;                 const int row = row0 + ai * HALF + m * 16; float ss = 0.f;
; #pragma unroll
;                 for (int bj = 0; bj < 2; ++bj) {
;                     const f32x4 v0 = bf2f_lo(old[m][bj], 0) + acc[ai][bj][m][0], v1 = bf2f_lo(old[m][bj], 1) + acc[ai][bj][m][1];
;                     ss += sumsq4(v0) + sumsq4(v1);
;                     *(u32x4*)(xb + (size_t)row * DM + col0 + bj * HALF) = pack8(v0, v1);
;                     { u32x2 w8; w8.x = pack4_fp8_x8(v0); w8.y = pack4_fp8_x8(v1); *(u32x2*)(xq + (size_t)row * DM + col0 + bj * HALF) = w8; }
;                 }
;                 ss = xor32_add(xor16_add(ss));
;                 if (fq == 0) ssx[(size_t)row * 16 + u.pn * 4 + wc] = ss;
.LBB0_1811:
	v_lshl_add_u32 v172, s61, 8, v163
	v_lshl_or_b32 v122, s60, 8, v193
	v_ashrrev_i32_e32 v123, 31, v122
	v_ashrrev_i32_e32 v173, 31, v172
	v_lshl_add_u64 v[174:175], v[122:123], 1, s[22:23]
	v_lshl_add_u64 v[170:171], s[24:25], 0, v[122:123]
	v_lshlrev_b64 v[122:123], 11, v[172:173]
	v_lshl_add_u64 v[190:191], v[174:175], 0, v[122:123]
	global_load_dwordx4 v[204:207], v[190:191], off
	global_load_dwordx4 v[154:157], v[190:191], off offset:256
	v_or_b32_e32 v184, 16, v172
	v_ashrrev_i32_e32 v185, 31, v184
	v_or_b32_e32 v180, 32, v172
	v_lshlrev_b64 v[122:123], 11, v[184:185]
	v_ashrrev_i32_e32 v181, 31, v180
	v_or_b32_e32 v176, 48, v172
	v_lshl_add_u64 v[186:187], v[174:175], 0, v[122:123]
	v_lshlrev_b64 v[122:123], 11, v[180:181]
	v_ashrrev_i32_e32 v177, 31, v176
	v_lshl_add_u64 v[182:183], v[174:175], 0, v[122:123]
	v_lshlrev_b64 v[122:123], 11, v[176:177]
	v_lshl_add_u64 v[178:179], v[174:175], 0, v[122:123]
	global_load_dwordx4 v[150:153], v[186:187], off
	global_load_dwordx4 v[146:149], v[186:187], off offset:256
	global_load_dwordx4 v[142:145], v[182:183], off
	global_load_dwordx4 v[138:141], v[182:183], off offset:256
	global_load_dwordx4 v[126:129], v[178:179], off
	global_load_dwordx4 v[122:125], v[178:179], off offset:256
	v_mov_b32_e32 v242, 0x40000
	v_mov_b32_e32 v243, 0
	v_lshl_add_u64 v[240:241], v[190:191], 0, v[242:243]
	global_load_dwordx4 v[208:211], v[240:241], off
	global_load_dwordx4 v[212:215], v[240:241], off offset:256
	v_lshl_add_u64 v[240:241], v[186:187], 0, v[242:243]
	global_load_dwordx4 v[216:219], v[240:241], off
	global_load_dwordx4 v[220:223], v[240:241], off offset:256
	v_lshl_add_u64 v[240:241], v[182:183], 0, v[242:243]
	global_load_dwordx4 v[224:227], v[240:241], off
	global_load_dwordx4 v[228:231], v[240:241], off offset:256
	v_lshl_add_u64 v[240:241], v[178:179], 0, v[242:243]
	global_load_dwordx4 v[232:235], v[240:241], off
	global_load_dwordx4 v[236:239], v[240:241], off offset:256
	v_lshlrev_b64 v[188:189], 10, v[172:173]
	v_lshl_add_u64 v[188:189], v[170:171], 0, v[188:189]
	s_lshl_b32 s28, s60, 2
	s_ashr_i32 s29, s28, 31
	s_lshl_b64 s[28:29], s[28:29], 2
	s_add_u32 s28, s49, s28
	s_addc_u32 s29, s50, s29
	s_waitcnt vmcnt(8)
	v_lshlrev_b32_e32 v196, 16, v204
	v_and_b32_e32 v197, 0xffff0000, v204
	v_lshlrev_b32_e32 v198, 16, v205
	v_and_b32_e32 v199, 0xffff0000, v205
	v_pk_add_f32 v[136:137], v[136:137], v[198:199]
	v_pk_add_f32 v[196:197], v[134:135], v[196:197]
	v_lshlrev_b32_e32 v134, 16, v206
	v_and_b32_e32 v135, 0xffff0000, v206
	v_lshlrev_b32_e32 v198, 16, v207
	v_and_b32_e32 v199, 0xffff0000, v207
	v_pk_add_f32 v[130:131], v[130:131], v[134:135]
	v_mul_f32_e32 v134, v197, v197
	v_mul_f32_e32 v135, v137, v137
	v_pk_add_f32 v[132:133], v[132:133], v[198:199]
	v_fmac_f32_e32 v134, v196, v196
	v_fmac_f32_e32 v135, v136, v136
	v_add_f32_e32 v134, v134, v135
	v_mul_f32_e32 v135, v131, v131
	v_mul_f32_e32 v195, v133, v133
	v_fmac_f32_e32 v135, v130, v130
	v_fmac_f32_e32 v195, v132, v132
	v_cvt_pk_bf16_f32 v204, v196, v197
	v_cvt_pk_bf16_f32 v205, v136, v137
	v_cvt_pk_bf16_f32 v206, v130, v131
	v_mul_f32_e32 v130, 0x41000000, v130
	v_mul_f32_e32 v131, 0x41000000, v131
	v_add_f32_e32 v135, v135, v195
	v_mul_f32_e32 v195, 0x41000000, v197
	v_med3_f32 v130, v130, s64, v250
	v_med3_f32 v131, v131, s64, v250
	v_mov_b32_e32 v197, v1
	v_cvt_pk_fp8_f32 v197, v130, v131
	v_add_f32_e32 v134, v134, v135
	v_mul_f32_e32 v135, 0x41000000, v196
	v_mul_f32_e32 v130, 0x41000000, v132
	v_mul_f32_e32 v131, 0x41000000, v133
	v_med3_f32 v135, v135, s64, v250
	v_med3_f32 v195, v195, s64, v250
	v_mov_b32_e32 v196, v1
	v_med3_f32 v130, v130, s64, v250
	v_med3_f32 v131, v131, s64, v250
	v_cvt_pk_bf16_f32 v207, v132, v133
	v_cvt_pk_fp8_f32 v196, v135, v195
	v_cvt_pk_fp8_f32 v197, v130, v131 op_sel:[0,0,1]
	v_lshlrev_b32_e32 v130, 16, v154
	v_and_b32_e32 v131, 0xffff0000, v154
	v_lshlrev_b32_e32 v132, 16, v155
	v_and_b32_e32 v133, 0xffff0000, v155
	v_pk_add_f32 v[120:121], v[120:121], v[132:133]
	v_pk_add_f32 v[118:119], v[118:119], v[130:131]
	v_lshlrev_b32_e32 v130, 16, v156
	v_and_b32_e32 v131, 0xffff0000, v156
	v_mul_f32_e32 v135, 0x41000000, v136
	v_mul_f32_e32 v136, 0x41000000, v137
	v_lshlrev_b32_e32 v132, 16, v157
	v_and_b32_e32 v133, 0xffff0000, v157
	v_pk_add_f32 v[130:131], v[114:115], v[130:131]
	v_mul_f32_e32 v114, v119, v119
	v_mul_f32_e32 v115, v121, v121
	v_med3_f32 v135, v135, s64, v250
	v_med3_f32 v136, v136, s64, v250
	v_pk_add_f32 v[132:133], v[116:117], v[132:133]
	v_fmac_f32_e32 v114, v118, v118
	v_fmac_f32_e32 v115, v120, v120
	v_cvt_pk_fp8_f32 v196, v135, v136 op_sel:[0,0,1]
	v_add_f32_e32 v114, v114, v115
	v_mul_f32_e32 v115, v131, v131
	v_mul_f32_e32 v116, v133, v133
	v_fmac_f32_e32 v115, v130, v130
	v_fmac_f32_e32 v116, v132, v132
	v_add_f32_e32 v115, v115, v116
	v_add_f32_e32 v114, v114, v115
	global_store_dwordx4 v[190:191], v[204:207], off
	global_store_dwordx2 v[188:189], v[196:197], off
	v_add_f32_e32 v134, v134, v114
	v_cvt_pk_bf16_f32 v114, v118, v119
	v_cvt_pk_bf16_f32 v115, v120, v121
	v_cvt_pk_bf16_f32 v116, v130, v131
	v_cvt_pk_bf16_f32 v117, v132, v133
	global_store_dwordx4 v[190:191], v[114:117], off offset:256
	s_nop 1
	v_mul_f32_e32 v114, 0x41000000, v118
	v_med3_f32 v115, v114, s64, v250
	v_mul_f32_e32 v114, 0x41000000, v119
	v_med3_f32 v116, v114, s64, v250
	v_mov_b32_e32 v114, v1
	v_cvt_pk_fp8_f32 v114, v115, v116
	v_mul_f32_e32 v115, 0x41000000, v120
	v_mul_f32_e32 v116, 0x41000000, v121
	v_med3_f32 v115, v115, s64, v250
	v_med3_f32 v116, v116, s64, v250
	v_cvt_pk_fp8_f32 v114, v115, v116 op_sel:[0,0,1]
	v_mul_f32_e32 v115, 0x41000000, v130
	v_med3_f32 v116, v115, s64, v250
	v_mul_f32_e32 v115, 0x41000000, v131
	v_med3_f32 v117, v115, s64, v250
	v_mov_b32_e32 v115, v1
	v_cvt_pk_fp8_f32 v115, v116, v117
	v_mul_f32_e32 v116, 0x41000000, v132
	v_mul_f32_e32 v117, 0x41000000, v133
	v_med3_f32 v116, v116, s64, v250
	v_med3_f32 v117, v117, s64, v250
	v_cvt_pk_fp8_f32 v115, v116, v117 op_sel:[0,0,1]
	global_store_dwordx2 v[188:189], v[114:115], off offset:128
	ds_swizzle_b32 v114, v134 offset:swizzle(SWAP,16)
	s_waitcnt lgkmcnt(0)
	v_add_f32_e32 v114, v134, v114
	v_mov_b32_e32 v115, v114
	s_nop 1
	v_permlane32_swap_b32_e32 v114, v115
	s_and_saveexec_b64 s[30:31], s[2:3]
	s_cbranch_execz .LBB0_1813
	v_lshlrev_b64 v[116:117], 6, v[172:173]
	v_lshl_add_u64 v[116:117], s[28:29], 0, v[116:117]
	v_add_f32_e32 v114, v114, v115
	global_store_dword v[116:117], v114, off

; __device__ __forceinline__ u32x4 pack8(const f32x4 a, const f32x4 b) { u32x4 w; w.x = cvt_pk_bf16(a[0], a[1]); w.y = cvt_pk_bf16(a[2], a[3]); w.z = cvt_pk_bf16(b[0], b[1]); w.w = cvt_pk_bf16(b[2], b[3]); return w; }
; __device__ __forceinline__ float sumsq4(const f32x4 v) { return (v[0] * v[0] + v[1] * v[1]) + (v[2] * v[2] + v[3] * v[3]); }
; __device__ __forceinline__ float xor16_add(float v) { return v + __int_as_float(__builtin_amdgcn_ds_swizzle(__float_as_int(v), 0x401F)); }
; __device__ __forceinline__ float xor32_add(float v) { auto rr = __builtin_amdgcn_permlane32_swap(__float_as_uint(v), __float_as_uint(v), false, false); return __uint_as_float(rr[0]) + __uint_as_float(rr[1]); }
; __device__ __forceinline__ f32x4 bf2f_lo(const u32x4 w, int h) { const unsigned a = h ? w.z : w.x, b = h ? w.w : w.y; return (f32x4){__uint_as_float(a << 16), __uint_as_float(a & 0xffff0000u), __uint_as_float(b << 16), __uint_as_float(b & 0xffff0000u)}; }
;     __device__ __forceinline__ void operator()(const f32x4 (&acc)[2][2][4][2], const Unit& u, int wr, int wc, int fr, int fq) const {
;     ...
;                 for (int bj = 0; bj < 2; ++bj) old[m][bj] = *(const u32x4*)(xb + (size_t)(row0 + ai * HALF + m * 16) * DM + col0 + bj * HALF);
; #pragma unroll
;             for (int m = 0; m < 4; ++m) {
;                 const int row = row0 + ai * HALF + m * 16; float ss = 0.f;
; #pragma unroll
;                 for (int bj = 0; bj < 2; ++bj) {
;                     const f32x4 v0 = bf2f_lo(old[m][bj], 0) + acc[ai][bj][m][0], v1 = bf2f_lo(old[m][bj], 1) + acc[ai][bj][m][1];
;                     ss += sumsq4(v0) + sumsq4(v1);
;                     *(u32x4*)(xb + (size_t)row * DM + col0 + bj * HALF) = pack8(v0, v1);
;                     { u32x2 w8; w8.x = pack4_fp8_x8(v0); w8.y = pack4_fp8_x8(v1); *(u32x2*)(xq + (size_t)row * DM + col0 + bj * HALF) = w8; }
;                 }
;                 ss = xor32_add(xor16_add(ss));
;                 if (fq == 0) ssx[(size_t)row * 16 + u.pn * 4 + wc] = ss;
.LBB0_1819:
	s_or_b64 exec, exec, s[30:31]
	v_add_u32_e32 v106, 0x80, v172
	v_ashrrev_i32_e32 v107, 31, v106
	v_lshlrev_b64 v[66:67], 11, v[106:107]
	v_lshl_add_u64 v[108:109], v[174:175], 0, v[66:67]
	v_add_u32_e32 v102, 0x90, v172
	v_ashrrev_i32_e32 v103, 31, v102
	v_add_u32_e32 v98, 0xa0, v172
	v_lshlrev_b64 v[66:67], 11, v[102:103]
	v_ashrrev_i32_e32 v99, 31, v98
	v_add_u32_e32 v94, 0xb0, v172
	v_lshl_add_u64 v[104:105], v[174:175], 0, v[66:67]
	v_lshlrev_b64 v[66:67], 11, v[98:99]
	v_ashrrev_i32_e32 v95, 31, v94
	v_lshl_add_u64 v[100:101], v[174:175], 0, v[66:67]
	v_lshlrev_b64 v[66:67], 11, v[94:95]
	v_lshl_add_u64 v[96:97], v[174:175], 0, v[66:67]
	s_waitcnt vmcnt(16)
	v_mov_b32_e32 v112, v208
	v_mov_b32_e32 v113, v209
	v_mov_b32_e32 v114, v210
	v_mov_b32_e32 v115, v211
	v_mov_b32_e32 v90, v212
	v_mov_b32_e32 v91, v213
	v_mov_b32_e32 v92, v214
	v_mov_b32_e32 v93, v215
	v_mov_b32_e32 v86, v216
	v_mov_b32_e32 v87, v217
	v_mov_b32_e32 v88, v218
	v_mov_b32_e32 v89, v219
	v_mov_b32_e32 v82, v220
	v_mov_b32_e32 v83, v221
	v_mov_b32_e32 v84, v222
	v_mov_b32_e32 v85, v223
	v_mov_b32_e32 v78, v224
	v_mov_b32_e32 v79, v225
	v_mov_b32_e32 v80, v226
	v_mov_b32_e32 v81, v227
	v_mov_b32_e32 v74, v228
	v_mov_b32_e32 v75, v229
	v_mov_b32_e32 v76, v230
	v_mov_b32_e32 v77, v231
	v_mov_b32_e32 v70, v232
	v_mov_b32_e32 v71, v233
	v_mov_b32_e32 v72, v234
	v_mov_b32_e32 v73, v235
	v_mov_b32_e32 v66, v236
	v_mov_b32_e32 v67, v237
	v_mov_b32_e32 v68, v238
	v_mov_b32_e32 v69, v239
	v_lshlrev_b64 v[110:111], 10, v[106:107]
	v_lshl_add_u64 v[110:111], v[170:171], 0, v[110:111]
	v_lshlrev_b32_e32 v116, 16, v112
	v_and_b32_e32 v117, 0xffff0000, v112
	v_lshlrev_b32_e32 v112, 16, v113
	v_and_b32_e32 v113, 0xffff0000, v113
	v_pk_add_f32 v[112:113], v[64:65], v[112:113]
	v_pk_add_f32 v[116:117], v[62:63], v[116:117]
	v_lshlrev_b32_e32 v62, 16, v114
	v_and_b32_e32 v63, 0xffff0000, v114
	v_lshlrev_b32_e32 v64, 16, v115
	v_and_b32_e32 v65, 0xffff0000, v115
	v_pk_add_f32 v[114:115], v[58:59], v[62:63]
	v_mul_f32_e32 v58, v117, v117
	v_mul_f32_e32 v59, v113, v113
	v_pk_add_f32 v[60:61], v[60:61], v[64:65]
	v_fmac_f32_e32 v58, v116, v116
	v_fmac_f32_e32 v59, v112, v112
	v_add_f32_e32 v58, v58, v59
	v_mul_f32_e32 v59, v115, v115
	v_mul_f32_e32 v62, v61, v61
	v_fmac_f32_e32 v59, v114, v114
	v_fmac_f32_e32 v62, v60, v60
	v_add_f32_e32 v59, v59, v62
	v_cvt_pk_bf16_f32 v62, v116, v117
	v_add_f32_e32 v58, v58, v59
	v_cvt_pk_bf16_f32 v63, v112, v113
	v_cvt_pk_bf16_f32 v64, v114, v115
	v_cvt_pk_bf16_f32 v65, v60, v61
	global_store_dwordx4 v[108:109], v[62:65], off
	v_mul_f32_e32 v59, 0x41000000, v116
	v_med3_f32 v59, v59, s64, v250
	v_mul_f32_e32 v62, 0x41000000, v117
	v_med3_f32 v63, v62, s64, v250
	v_mov_b32_e32 v62, v1
	v_cvt_pk_fp8_f32 v62, v59, v63
	v_mul_f32_e32 v59, 0x41000000, v112
	v_mul_f32_e32 v63, 0x41000000, v113
	v_med3_f32 v59, v59, s64, v250
	v_med3_f32 v63, v63, s64, v250
	v_cvt_pk_fp8_f32 v62, v59, v63 op_sel:[0,0,1]
	v_mul_f32_e32 v59, 0x41000000, v114
	v_mul_f32_e32 v63, 0x41000000, v115
	v_med3_f32 v59, v59, s64, v250
	v_med3_f32 v64, v63, s64, v250
	v_mov_b32_e32 v63, v1
	v_cvt_pk_fp8_f32 v63, v59, v64
	v_mul_f32_e32 v59, 0x41000000, v60
	v_mul_f32_e32 v60, 0x41000000, v61
	v_med3_f32 v59, v59, s64, v250
	v_med3_f32 v60, v60, s64, v250
	v_cvt_pk_fp8_f32 v63, v59, v60 op_sel:[0,0,1]
	v_lshlrev_b32_e32 v60, 16, v90
	v_and_b32_e32 v61, 0xffff0000, v90
	v_pk_add_f32 v[54:55], v[54:55], v[60:61]
	global_store_dwordx2 v[110:111], v[62:63], off
	v_lshlrev_b32_e32 v62, 16, v91
	v_and_b32_e32 v63, 0xffff0000, v91
	v_pk_add_f32 v[56:57], v[56:57], v[62:63]
	v_lshlrev_b32_e32 v60, 16, v92
	v_and_b32_e32 v61, 0xffff0000, v92
	v_lshlrev_b32_e32 v62, 16, v93
	v_and_b32_e32 v63, 0xffff0000, v93
	v_pk_add_f32 v[60:61], v[50:51], v[60:61]
	v_mul_f32_e32 v50, v55, v55
	v_mul_f32_e32 v51, v57, v57
	v_pk_add_f32 v[62:63], v[52:53], v[62:63]
	v_fmac_f32_e32 v50, v54, v54
	v_fmac_f32_e32 v51, v56, v56
	v_add_f32_e32 v50, v50, v51
	v_mul_f32_e32 v51, v61, v61
	v_mul_f32_e32 v52, v63, v63
	v_fmac_f32_e32 v51, v60, v60
	v_fmac_f32_e32 v52, v62, v62
	v_add_f32_e32 v51, v51, v52
	v_add_f32_e32 v50, v50, v51
	v_add_f32_e32 v58, v58, v50
	v_cvt_pk_bf16_f32 v50, v54, v55
	v_cvt_pk_bf16_f32 v51, v56, v57
	v_cvt_pk_bf16_f32 v52, v60, v61
	v_cvt_pk_bf16_f32 v53, v62, v63
	global_store_dwordx4 v[108:109], v[50:53], off offset:256
	s_nop 1
	v_mul_f32_e32 v50, 0x41000000, v54
	v_med3_f32 v51, v50, s64, v250
	v_mul_f32_e32 v50, 0x41000000, v55
	v_med3_f32 v52, v50, s64, v250
	v_mov_b32_e32 v50, v1
	v_cvt_pk_fp8_f32 v50, v51, v52
	v_mul_f32_e32 v51, 0x41000000, v56
	v_mul_f32_e32 v52, 0x41000000, v57
	v_med3_f32 v51, v51, s64, v250
	v_med3_f32 v52, v52, s64, v250
	v_cvt_pk_fp8_f32 v50, v51, v52 op_sel:[0,0,1]
	v_mul_f32_e32 v51, 0x41000000, v60
	v_med3_f32 v52, v51, s64, v250
	v_mul_f32_e32 v51, 0x41000000, v61
	v_med3_f32 v53, v51, s64, v250
	v_mov_b32_e32 v51, v1
	v_cvt_pk_fp8_f32 v51, v52, v53
	v_mul_f32_e32 v52, 0x41000000, v62
	v_mul_f32_e32 v53, 0x41000000, v63
	v_med3_f32 v52, v52, s64, v250
	v_med3_f32 v53, v53, s64, v250
	v_cvt_pk_fp8_f32 v51, v52, v53 op_sel:[0,0,1]
	global_store_dwordx2 v[110:111], v[50:51], off offset:128
	ds_swizzle_b32 v50, v58 offset:swizzle(SWAP,16)
	s_waitcnt lgkmcnt(0)
	v_add_f32_e32 v50, v58, v50
	v_mov_b32_e32 v51, v50
	s_nop 1
	v_permlane32_swap_b32_e32 v50, v51
	s_and_saveexec_b64 s[30:31], s[2:3]
	s_cbranch_execz .LBB0_1821
	v_lshlrev_b64 v[52:53], 6, v[106:107]
	v_lshl_add_u64 v[52:53], s[28:29], 0, v[52:53]
	v_add_f32_e32 v50, v50, v51
	global_store_dword v[52:53], v50, off
; __device__ __forceinline__ u32x4 pack8(const f32x4 a, const f32x4 b) { u32x4 w; w.x = cvt_pk_bf16(a[0], a[1]); w.y = cvt_pk_bf16(a[2], a[3]); w.z = cvt_pk_bf16(b[0], b[1]); w.w = cvt_pk_bf16(b[2], b[3]); return w; }
; __device__ __forceinline__ float sumsq4(const f32x4 v) { return (v[0] * v[0] + v[1] * v[1]) + (v[2] * v[2] + v[3] * v[3]); }
; __device__ __forceinline__ float xor16_add(float v) { return v + __int_as_float(__builtin_amdgcn_ds_swizzle(__float_as_int(v), 0x401F)); }
; __device__ __forceinline__ float xor32_add(float v) { auto rr = __builtin_amdgcn_permlane32_swap(__float_as_uint(v), __float_as_uint(v), false, false); return __uint_as_float(rr[0]) + __uint_as_float(rr[1]); }
; __device__ __forceinline__ f32x4 bf2f_lo(const u32x4 w, int h) { const unsigned a = h ? w.z : w.x, b = h ? w.w : w.y; return (f32x4){__uint_as_float(a << 16), __uint_as_float(a & 0xffff0000u), __uint_as_float(b << 16), __uint_as_float(b & 0xffff0000u)}; }
;     __device__ __forceinline__ void operator()(const f32x4 (&acc)[2][2][4][2], const Unit& u, int wr, int wc, int fr, int fq) const {
;     ...
;             for (int m = 0; m < 4; ++m) {
;                 const int row = row0 + ai * HALF + m * 16; float ss = 0.f;
; #pragma unroll
;                 for (int bj = 0; bj < 2; ++bj) {
;                     const f32x4 v0 = bf2f_lo(old[m][bj], 0) + acc[ai][bj][m][0], v1 = bf2f_lo(old[m][bj], 1) + acc[ai][bj][m][1];
;                     ss += sumsq4(v0) + sumsq4(v1);
;                     *(u32x4*)(xb + (size_t)row * DM + col0 + bj * HALF) = pack8(v0, v1);
;                     { u32x2 w8; w8.x = pack4_fp8_x8(v0); w8.y = pack4_fp8_x8(v1); *(u32x2*)(xq + (size_t)row * DM + col0 + bj * HALF) = w8; }
;                 }
;                 ss = xor32_add(xor16_add(ss));
;                 if (fq == 0) ssx[(size_t)row * 16 + u.pn * 4 + wc] = ss;
.LBB0_1821:
	s_or_b64 exec, exec, s[30:31]
	v_lshlrev_b32_e32 v52, 16, v86
	v_and_b32_e32 v53, 0xffff0000, v86
	v_lshlrev_b32_e32 v54, 16, v87
	v_and_b32_e32 v55, 0xffff0000, v87
	v_pk_add_f32 v[48:49], v[48:49], v[54:55]
	v_pk_add_f32 v[46:47], v[46:47], v[52:53]
	v_lshlrev_b32_e32 v52, 16, v88
	v_and_b32_e32 v53, 0xffff0000, v88
	v_lshlrev_b32_e32 v54, 16, v89
	v_and_b32_e32 v55, 0xffff0000, v89
	v_pk_add_f32 v[54:55], v[44:45], v[54:55]
	v_pk_add_f32 v[44:45], v[42:43], v[52:53]
	v_mul_f32_e32 v42, v47, v47
	v_mul_f32_e32 v43, v49, v49
	v_fmac_f32_e32 v42, v46, v46
	v_fmac_f32_e32 v43, v48, v48
	v_add_f32_e32 v42, v42, v43
	v_mul_f32_e32 v43, v45, v45
	v_mul_f32_e32 v52, v55, v55
	v_fmac_f32_e32 v43, v44, v44
	v_fmac_f32_e32 v52, v54, v54
	v_add_f32_e32 v43, v43, v52
	v_add_f32_e32 v52, v42, v43
	v_cvt_pk_bf16_f32 v42, v46, v47
	v_mul_f32_e32 v46, 0x41000000, v46
	v_med3_f32 v53, v46, s64, v250
	v_mul_f32_e32 v46, 0x41000000, v47
	v_med3_f32 v47, v46, s64, v250
	v_mov_b32_e32 v46, v1
	v_cvt_pk_fp8_f32 v46, v53, v47
	v_cvt_pk_bf16_f32 v43, v48, v49
	v_mul_f32_e32 v47, 0x41000000, v48
	v_mul_f32_e32 v48, 0x41000000, v49
	v_med3_f32 v47, v47, s64, v250
	v_med3_f32 v48, v48, s64, v250
	v_cvt_pk_fp8_f32 v46, v47, v48 op_sel:[0,0,1]
	v_mul_f32_e32 v47, 0x41000000, v44
	v_med3_f32 v48, v47, s64, v250
	v_mul_f32_e32 v47, 0x41000000, v45
	v_med3_f32 v49, v47, s64, v250
	v_mov_b32_e32 v47, v1
	v_cvt_pk_fp8_f32 v47, v48, v49
	v_mul_f32_e32 v48, 0x41000000, v54
	v_mul_f32_e32 v49, 0x41000000, v55
	v_med3_f32 v48, v48, s64, v250
	v_med3_f32 v49, v49, s64, v250
	v_cvt_pk_fp8_f32 v47, v48, v49 op_sel:[0,0,1]
	v_lshlrev_b64 v[50:51], 10, v[102:103]
	v_cvt_pk_bf16_f32 v44, v44, v45
	v_cvt_pk_bf16_f32 v45, v54, v55
	v_lshl_add_u64 v[50:51], v[170:171], 0, v[50:51]
	global_store_dwordx4 v[104:105], v[42:45], off
	global_store_dwordx2 v[50:51], v[46:47], off
	v_lshlrev_b32_e32 v42, 16, v82
	v_and_b32_e32 v43, 0xffff0000, v82
	v_lshlrev_b32_e32 v44, 16, v83
	v_and_b32_e32 v45, 0xffff0000, v83
	v_pk_add_f32 v[40:41], v[40:41], v[44:45]
	v_pk_add_f32 v[38:39], v[38:39], v[42:43]
	v_lshlrev_b32_e32 v42, 16, v84
	v_and_b32_e32 v43, 0xffff0000, v84
	v_lshlrev_b32_e32 v44, 16, v85
	v_and_b32_e32 v45, 0xffff0000, v85
	v_pk_add_f32 v[44:45], v[36:37], v[44:45]
	v_pk_add_f32 v[36:37], v[34:35], v[42:43]
	v_mul_f32_e32 v34, v39, v39
	v_mul_f32_e32 v35, v41, v41
	v_fmac_f32_e32 v34, v38, v38
	v_fmac_f32_e32 v35, v40, v40
	v_add_f32_e32 v34, v34, v35
	v_mul_f32_e32 v35, v37, v37
	v_mul_f32_e32 v42, v45, v45
	v_fmac_f32_e32 v35, v36, v36
	v_fmac_f32_e32 v42, v44, v44
	v_add_f32_e32 v35, v35, v42
	v_add_f32_e32 v34, v34, v35
	v_add_f32_e32 v42, v52, v34
	v_cvt_pk_bf16_f32 v34, v38, v39
	v_mul_f32_e32 v38, 0x41000000, v38
	v_med3_f32 v43, v38, s64, v250
	v_mul_f32_e32 v38, 0x41000000, v39
	v_med3_f32 v39, v38, s64, v250
	v_mov_b32_e32 v38, v1
	v_cvt_pk_fp8_f32 v38, v43, v39
	v_cvt_pk_bf16_f32 v35, v40, v41
	v_mul_f32_e32 v39, 0x41000000, v40
	v_mul_f32_e32 v40, 0x41000000, v41
	v_med3_f32 v39, v39, s64, v250
	v_med3_f32 v40, v40, s64, v250
	v_cvt_pk_fp8_f32 v38, v39, v40 op_sel:[0,0,1]
	v_mul_f32_e32 v39, 0x41000000, v36
	v_med3_f32 v40, v39, s64, v250
	v_mul_f32_e32 v39, 0x41000000, v37
	v_med3_f32 v41, v39, s64, v250
	v_mov_b32_e32 v39, v1
	v_cvt_pk_fp8_f32 v39, v40, v41
	v_mul_f32_e32 v40, 0x41000000, v44
	v_mul_f32_e32 v41, 0x41000000, v45
	v_med3_f32 v40, v40, s64, v250
	v_med3_f32 v41, v41, s64, v250
	v_cvt_pk_fp8_f32 v39, v40, v41 op_sel:[0,0,1]
	ds_swizzle_b32 v40, v42 offset:swizzle(SWAP,16)
	v_cvt_pk_bf16_f32 v36, v36, v37
	v_cvt_pk_bf16_f32 v37, v44, v45
	global_store_dwordx4 v[104:105], v[34:37], off offset:256
	global_store_dwordx2 v[50:51], v[38:39], off offset:128
	s_waitcnt lgkmcnt(0)
	v_add_f32_e32 v34, v42, v40
	v_mov_b32_e32 v35, v34
	s_nop 1
	v_permlane32_swap_b32_e32 v34, v35
	s_and_saveexec_b64 s[30:31], s[2:3]
	s_cbranch_execz .LBB0_1823
	v_lshlrev_b64 v[36:37], 6, v[102:103]
	v_lshl_add_u64 v[36:37], s[28:29], 0, v[36:37]
	v_add_f32_e32 v34, v34, v35
	global_store_dword v[36:37], v34, off
.LBB0_1823:
	s_or_b64 exec, exec, s[30:31]
	v_lshlrev_b32_e32 v36, 16, v78
	v_and_b32_e32 v37, 0xffff0000, v78
	v_lshlrev_b32_e32 v38, 16, v79
	v_and_b32_e32 v39, 0xffff0000, v79
	v_pk_add_f32 v[32:33], v[32:33], v[38:39]
	v_pk_add_f32 v[30:31], v[30:31], v[36:37]
	v_lshlrev_b32_e32 v36, 16, v80
	v_and_b32_e32 v37, 0xffff0000, v80
	v_lshlrev_b32_e32 v38, 16, v81
	v_and_b32_e32 v39, 0xffff0000, v81
	v_pk_add_f32 v[38:39], v[28:29], v[38:39]
	v_pk_add_f32 v[28:29], v[26:27], v[36:37]
	v_mul_f32_e32 v26, v31, v31
	v_mul_f32_e32 v27, v33, v33
	v_fmac_f32_e32 v26, v30, v30
	v_fmac_f32_e32 v27, v32, v32
	v_add_f32_e32 v26, v26, v27
	v_mul_f32_e32 v27, v29, v29
	v_mul_f32_e32 v36, v39, v39
	v_fmac_f32_e32 v27, v28, v28
	v_fmac_f32_e32 v36, v38, v38
	v_add_f32_e32 v27, v27, v36
	v_add_f32_e32 v36, v26, v27
	v_cvt_pk_bf16_f32 v26, v30, v31
	v_mul_f32_e32 v30, 0x41000000, v30
	v_med3_f32 v37, v30, s64, v250
	v_mul_f32_e32 v30, 0x41000000, v31
	v_med3_f32 v31, v30, s64, v250
	v_mov_b32_e32 v30, v1
	v_cvt_pk_fp8_f32 v30, v37, v31
	v_cvt_pk_bf16_f32 v27, v32, v33
	v_mul_f32_e32 v31, 0x41000000, v32
	v_mul_f32_e32 v32, 0x41000000, v33
	v_med3_f32 v31, v31, s64, v250
	v_med3_f32 v32, v32, s64, v250
	v_cvt_pk_fp8_f32 v30, v31, v32 op_sel:[0,0,1]
	v_mul_f32_e32 v31, 0x41000000, v28
	v_med3_f32 v32, v31, s64, v250
	v_mul_f32_e32 v31, 0x41000000, v29
	v_med3_f32 v33, v31, s64, v250
	v_mov_b32_e32 v31, v1
	v_cvt_pk_fp8_f32 v31, v32, v33
	v_mul_f32_e32 v32, 0x41000000, v38
	v_mul_f32_e32 v33, 0x41000000, v39
	v_med3_f32 v32, v32, s64, v250
	v_med3_f32 v33, v33, s64, v250
; __device__ __forceinline__ u32x4 pack8(const f32x4 a, const f32x4 b) { u32x4 w; w.x = cvt_pk_bf16(a[0], a[1]); w.y = cvt_pk_bf16(a[2], a[3]); w.z = cvt_pk_bf16(b[0], b[1]); w.w = cvt_pk_bf16(b[2], b[3]); return w; }
; __device__ __forceinline__ float sumsq4(const f32x4 v) { return (v[0] * v[0] + v[1] * v[1]) + (v[2] * v[2] + v[3] * v[3]); }
; __device__ __forceinline__ float xor16_add(float v) { return v + __int_as_float(__builtin_amdgcn_ds_swizzle(__float_as_int(v), 0x401F)); }
; __device__ __forceinline__ float xor32_add(float v) { auto rr = __builtin_amdgcn_permlane32_swap(__float_as_uint(v), __float_as_uint(v), false, false); return __uint_as_float(rr[0]) + __uint_as_float(rr[1]); }
; __device__ __forceinline__ f32x4 bf2f_lo(const u32x4 w, int h) { const unsigned a = h ? w.z : w.x, b = h ? w.w : w.y; return (f32x4){__uint_as_float(a << 16), __uint_as_float(a & 0xffff0000u), __uint_as_float(b << 16), __uint_as_float(b & 0xffff0000u)}; }
;     __device__ __forceinline__ void operator()(const f32x4 (&acc)[2][2][4][2], const Unit& u, int wr, int wc, int fr, int fq) const {
;     ...
;             for (int m = 0; m < 4; ++m) {
;                 const int row = row0 + ai * HALF + m * 16; float ss = 0.f;
; #pragma unroll
;                 for (int bj = 0; bj < 2; ++bj) {
;                     const f32x4 v0 = bf2f_lo(old[m][bj], 0) + acc[ai][bj][m][0], v1 = bf2f_lo(old[m][bj], 1) + acc[ai][bj][m][1];
;                     ss += sumsq4(v0) + sumsq4(v1);
;                     *(u32x4*)(xb + (size_t)row * DM + col0 + bj * HALF) = pack8(v0, v1);
;                     { u32x2 w8; w8.x = pack4_fp8_x8(v0); w8.y = pack4_fp8_x8(v1); *(u32x2*)(xq + (size_t)row * DM + col0 + bj * HALF) = w8; }
;                 }
;                 ss = xor32_add(xor16_add(ss));
;                 if (fq == 0) ssx[(size_t)row * 16 + u.pn * 4 + wc] = ss;
	v_cvt_pk_fp8_f32 v31, v32, v33 op_sel:[0,0,1]
	v_lshlrev_b64 v[34:35], 10, v[98:99]
	v_cvt_pk_bf16_f32 v28, v28, v29
	v_cvt_pk_bf16_f32 v29, v38, v39
	v_lshl_add_u64 v[34:35], v[170:171], 0, v[34:35]
	global_store_dwordx4 v[100:101], v[26:29], off
	global_store_dwordx2 v[34:35], v[30:31], off
	v_lshlrev_b32_e32 v26, 16, v74
	v_and_b32_e32 v27, 0xffff0000, v74
	v_lshlrev_b32_e32 v28, 16, v75
	v_and_b32_e32 v29, 0xffff0000, v75
	v_pk_add_f32 v[24:25], v[24:25], v[28:29]
	v_pk_add_f32 v[22:23], v[22:23], v[26:27]
	v_lshlrev_b32_e32 v26, 16, v76
	v_and_b32_e32 v27, 0xffff0000, v76
	v_lshlrev_b32_e32 v28, 16, v77
	v_and_b32_e32 v29, 0xffff0000, v77
	v_pk_add_f32 v[28:29], v[20:21], v[28:29]
	v_pk_add_f32 v[20:21], v[18:19], v[26:27]
	v_mul_f32_e32 v18, v23, v23
	v_mul_f32_e32 v19, v25, v25
	v_fmac_f32_e32 v18, v22, v22
	v_fmac_f32_e32 v19, v24, v24
	v_add_f32_e32 v18, v18, v19
	v_mul_f32_e32 v19, v21, v21
	v_mul_f32_e32 v26, v29, v29
	v_fmac_f32_e32 v19, v20, v20
	v_fmac_f32_e32 v26, v28, v28
	v_add_f32_e32 v19, v19, v26
	v_add_f32_e32 v18, v18, v19
	v_add_f32_e32 v26, v36, v18
	v_cvt_pk_bf16_f32 v18, v22, v23
	v_mul_f32_e32 v22, 0x41000000, v22
	v_med3_f32 v27, v22, s64, v250
	v_mul_f32_e32 v22, 0x41000000, v23
	v_med3_f32 v23, v22, s64, v250
	v_mov_b32_e32 v22, v1
	v_cvt_pk_fp8_f32 v22, v27, v23
	v_cvt_pk_bf16_f32 v19, v24, v25
	v_mul_f32_e32 v23, 0x41000000, v24
	v_mul_f32_e32 v24, 0x41000000, v25
	v_med3_f32 v23, v23, s64, v250
	v_med3_f32 v24, v24, s64, v250
	v_cvt_pk_fp8_f32 v22, v23, v24 op_sel:[0,0,1]
	v_mul_f32_e32 v23, 0x41000000, v20
	v_med3_f32 v24, v23, s64, v250
	v_mul_f32_e32 v23, 0x41000000, v21
	v_med3_f32 v25, v23, s64, v250
	v_mov_b32_e32 v23, v1
	v_cvt_pk_fp8_f32 v23, v24, v25
	v_mul_f32_e32 v24, 0x41000000, v28
	v_mul_f32_e32 v25, 0x41000000, v29
	v_med3_f32 v24, v24, s64, v250
	v_med3_f32 v25, v25, s64, v250
	v_cvt_pk_fp8_f32 v23, v24, v25 op_sel:[0,0,1]
	ds_swizzle_b32 v24, v26 offset:swizzle(SWAP,16)
	v_cvt_pk_bf16_f32 v20, v20, v21
	v_cvt_pk_bf16_f32 v21, v28, v29
	global_store_dwordx4 v[100:101], v[18:21], off offset:256
	global_store_dwordx2 v[34:35], v[22:23], off offset:128
	s_waitcnt lgkmcnt(0)
	v_add_f32_e32 v18, v26, v24
	v_mov_b32_e32 v19, v18
	s_nop 1
	v_permlane32_swap_b32_e32 v18, v19
	s_and_saveexec_b64 s[30:31], s[2:3]
	s_cbranch_execz .LBB0_1825
	v_lshlrev_b64 v[20:21], 6, v[98:99]
	v_lshl_add_u64 v[20:21], s[28:29], 0, v[20:21]
	v_add_f32_e32 v18, v18, v19
	global_store_dword v[20:21], v18, off
.LBB0_1825:
	s_or_b64 exec, exec, s[30:31]
	v_lshlrev_b32_e32 v20, 16, v70
	v_and_b32_e32 v21, 0xffff0000, v70
	v_lshlrev_b32_e32 v22, 16, v71
	v_and_b32_e32 v23, 0xffff0000, v71
	v_pk_add_f32 v[16:17], v[16:17], v[22:23]
	v_pk_add_f32 v[14:15], v[14:15], v[20:21]
	v_lshlrev_b32_e32 v20, 16, v72
	v_and_b32_e32 v21, 0xffff0000, v72
	v_lshlrev_b32_e32 v22, 16, v73
	v_and_b32_e32 v23, 0xffff0000, v73
	v_pk_add_f32 v[22:23], v[12:13], v[22:23]
	v_pk_add_f32 v[12:13], v[10:11], v[20:21]
	v_mul_f32_e32 v10, v15, v15
	v_mul_f32_e32 v11, v17, v17
	v_fmac_f32_e32 v10, v14, v14
	v_fmac_f32_e32 v11, v16, v16
	v_add_f32_e32 v10, v10, v11
	v_mul_f32_e32 v11, v13, v13
	v_mul_f32_e32 v20, v23, v23
	v_fmac_f32_e32 v11, v12, v12
	v_fmac_f32_e32 v20, v22, v22
	v_add_f32_e32 v11, v11, v20
	v_add_f32_e32 v20, v10, v11
	v_cvt_pk_bf16_f32 v10, v14, v15
	v_mul_f32_e32 v14, 0x41000000, v14
	v_med3_f32 v21, v14, s64, v250
	v_mul_f32_e32 v14, 0x41000000, v15
	v_med3_f32 v15, v14, s64, v250
	v_mov_b32_e32 v14, v1
	v_cvt_pk_fp8_f32 v14, v21, v15
	v_cvt_pk_bf16_f32 v11, v16, v17
	v_mul_f32_e32 v15, 0x41000000, v16
	v_mul_f32_e32 v16, 0x41000000, v17
	v_med3_f32 v15, v15, s64, v250
	v_med3_f32 v16, v16, s64, v250
	v_cvt_pk_fp8_f32 v14, v15, v16 op_sel:[0,0,1]
	v_mul_f32_e32 v15, 0x41000000, v12
	v_med3_f32 v16, v15, s64, v250
	v_mul_f32_e32 v15, 0x41000000, v13
	v_med3_f32 v17, v15, s64, v250
	v_mov_b32_e32 v15, v1
	v_cvt_pk_fp8_f32 v15, v16, v17
	v_mul_f32_e32 v16, 0x41000000, v22
	v_mul_f32_e32 v17, 0x41000000, v23
	v_med3_f32 v16, v16, s64, v250
	v_med3_f32 v17, v17, s64, v250
	v_cvt_pk_fp8_f32 v15, v16, v17 op_sel:[0,0,1]
	v_lshlrev_b64 v[18:19], 10, v[94:95]
	v_cvt_pk_bf16_f32 v12, v12, v13
	v_cvt_pk_bf16_f32 v13, v22, v23
	v_lshl_add_u64 v[18:19], v[170:171], 0, v[18:19]
	global_store_dwordx4 v[96:97], v[10:13], off
	global_store_dwordx2 v[18:19], v[14:15], off
	v_lshlrev_b32_e32 v10, 16, v66
	v_and_b32_e32 v11, 0xffff0000, v66
	v_lshlrev_b32_e32 v12, 16, v67
	v_and_b32_e32 v13, 0xffff0000, v67
	v_pk_add_f32 v[8:9], v[8:9], v[12:13]
	v_pk_add_f32 v[6:7], v[6:7], v[10:11]
	v_lshlrev_b32_e32 v10, 16, v68
	v_and_b32_e32 v11, 0xffff0000, v68
	v_lshlrev_b32_e32 v12, 16, v69
	v_and_b32_e32 v13, 0xffff0000, v69
	v_pk_add_f32 v[12:13], v[4:5], v[12:13]
	v_pk_add_f32 v[4:5], v[2:3], v[10:11]
	v_mul_f32_e32 v2, v7, v7
	v_mul_f32_e32 v3, v9, v9
	v_fmac_f32_e32 v2, v6, v6
	v_fmac_f32_e32 v3, v8, v8
	v_add_f32_e32 v2, v2, v3
	v_mul_f32_e32 v3, v5, v5
	v_mul_f32_e32 v10, v13, v13
	v_fmac_f32_e32 v3, v4, v4
	v_fmac_f32_e32 v10, v12, v12
	v_add_f32_e32 v3, v3, v10
	v_add_f32_e32 v2, v2, v3
	v_add_f32_e32 v10, v20, v2
	v_cvt_pk_bf16_f32 v2, v6, v7
	v_mul_f32_e32 v6, 0x41000000, v6
	v_med3_f32 v11, v6, s64, v250
	v_mul_f32_e32 v6, 0x41000000, v7
	v_med3_f32 v7, v6, s64, v250
	v_mov_b32_e32 v6, v1
	v_cvt_pk_fp8_f32 v6, v11, v7
	v_cvt_pk_bf16_f32 v3, v8, v9
	v_mul_f32_e32 v7, 0x41000000, v8
	v_mul_f32_e32 v8, 0x41000000, v9
	v_med3_f32 v7, v7, s64, v250
	v_med3_f32 v8, v8, s64, v250
	v_cvt_pk_fp8_f32 v6, v7, v8 op_sel:[0,0,1]
	v_mul_f32_e32 v7, 0x41000000, v4
	v_med3_f32 v8, v7, s64, v250
	v_mul_f32_e32 v7, 0x41000000, v5
	v_med3_f32 v9, v7, s64, v250
	v_mov_b32_e32 v7, v1
	v_cvt_pk_fp8_f32 v7, v8, v9
	v_mul_f32_e32 v8, 0x41000000, v12
	v_mul_f32_e32 v9, 0x41000000, v13
	v_med3_f32 v8, v8, s64, v250
	v_med3_f32 v9, v9, s64, v250
	v_cvt_pk_fp8_f32 v7, v8, v9 op_sel:[0,0,1]
	ds_swizzle_b32 v8, v10 offset:swizzle(SWAP,16)
	v_cvt_pk_bf16_f32 v4, v4, v5
	v_cvt_pk_bf16_f32 v5, v12, v13
	global_store_dwordx4 v[96:97], v[2:5], off offset:256
	global_store_dwordx2 v[18:19], v[6:7], off offset:128
	s_waitcnt lgkmcnt(0)
	v_add_f32_e32 v2, v10, v8
	v_mov_b32_e32 v3, v2
	s_nop 1
	v_permlane32_swap_b32_e32 v2, v3
	s_and_saveexec_b64 s[30:31], s[2:3]
	s_cbranch_execz .LBB0_1827
	v_lshlrev_b64 v[4:5], 6, v[94:95]
	v_lshl_add_u64 v[4:5], s[28:29], 0, v[4:5]
	v_add_f32_e32 v2, v2, v3
	global_store_dword v[4:5], v2, off

; __device__ __forceinline__ u32x4 pack8(const f32x4 a, const f32x4 b) { u32x4 w; w.x = cvt_pk_bf16(a[0], a[1]); w.y = cvt_pk_bf16(a[2], a[3]); w.z = cvt_pk_bf16(b[0], b[1]); w.w = cvt_pk_bf16(b[2], b[3]); return w; }
; __device__ __forceinline__ float sumsq4(const f32x4 v) { return (v[0] * v[0] + v[1] * v[1]) + (v[2] * v[2] + v[3] * v[3]); }
; __device__ __forceinline__ float xor16_add(float v) { return v + __int_as_float(__builtin_amdgcn_ds_swizzle(__float_as_int(v), 0x401F)); }
; __device__ __forceinline__ float xor32_add(float v) { auto rr = __builtin_amdgcn_permlane32_swap(__float_as_uint(v), __float_as_uint(v), false, false); return __uint_as_float(rr[0]) + __uint_as_float(rr[1]); }
; __device__ __forceinline__ f32x4 bf2f_lo(const u32x4 w, int h) { const unsigned a = h ? w.z : w.x, b = h ? w.w : w.y; return (f32x4){__uint_as_float(a << 16), __uint_as_float(a & 0xffff0000u), __uint_as_float(b << 16), __uint_as_float(b & 0xffff0000u)}; }
;     __device__ __forceinline__ void operator()(const f32x4 (&acc)[2][2][4][2], const Unit& u, int wr, int wc, int fr, int fq) const {
;     ...
;         const int row0 = u.pm * BM + wr * 64 + fr, col0 = u.pn * BM + wc * 32 + 8 * fq;
; #pragma unroll
;         for (int ai = 0; ai < 2; ++ai) {
;             u32x4 old[4][2];
; #pragma unroll
;             for (int m = 0; m < 4; ++m)
; #pragma unroll
;                 for (int bj = 0; bj < 2; ++bj) old[m][bj] = *(const u32x4*)(xb + (size_t)(row0 + ai * HALF + m * 16) * DM + col0 + bj * HALF);
; #pragma unroll
;             for (int m = 0; m < 4; ++m) {
;                 const int row = row0 + ai * HALF + m * 16; float ss = 0.f;
; #pragma unroll
;                 for (int bj = 0; bj < 2; ++bj) {
;                     const f32x4 v0 = bf2f_lo(old[m][bj], 0) + acc[ai][bj][m][0], v1 = bf2f_lo(old[m][bj], 1) + acc[ai][bj][m][1];
;                     ss += sumsq4(v0) + sumsq4(v1);
;                     *(u32x4*)(xb + (size_t)row * DM + col0 + bj * HALF) = pack8(v0, v1);
;                     { u32x2 w8; w8.x = pack4_fp8_x8(v0); w8.y = pack4_fp8_x8(v1); *(u32x2*)(xq + (size_t)row * DM + col0 + bj * HALF) = w8; }
;                 }
;                 ss = xor32_add(xor16_add(ss));
;                 if (fq == 0) ssx[(size_t)row * 16 + u.pn * 4 + wc] = ss;
.LBB0_1861:
	v_lshl_add_u32 v32, s61, 8, v163
	v_lshl_or_b32 v2, s60, 8, v193
	v_ashrrev_i32_e32 v3, 31, v2
	v_ashrrev_i32_e32 v33, 31, v32
	v_lshl_add_u64 v[174:175], v[2:3], 1, s[22:23]
	v_lshl_add_u64 v[30:31], s[24:25], 0, v[2:3]
	v_lshlrev_b64 v[2:3], 11, v[32:33]
	s_nop 15
	s_nop 15
	v_lshl_add_u64 v[190:191], v[174:175], 0, v[2:3]
	global_load_dwordx4 v[204:207], v[190:191], off
	global_load_dwordx4 v[26:29], v[190:191], off offset:256
	v_or_b32_e32 v184, 16, v32
	v_ashrrev_i32_e32 v185, 31, v184
	v_or_b32_e32 v180, 32, v32
	v_lshlrev_b64 v[2:3], 11, v[184:185]
	v_ashrrev_i32_e32 v181, 31, v180
	v_or_b32_e32 v176, 48, v32
	v_lshl_add_u64 v[186:187], v[174:175], 0, v[2:3]
	v_lshlrev_b64 v[2:3], 11, v[180:181]
	v_ashrrev_i32_e32 v177, 31, v176
	v_lshl_add_u64 v[182:183], v[174:175], 0, v[2:3]
	v_lshlrev_b64 v[2:3], 11, v[176:177]
	v_lshl_add_u64 v[178:179], v[174:175], 0, v[2:3]
	global_load_dwordx4 v[22:25], v[186:187], off
	global_load_dwordx4 v[18:21], v[186:187], off offset:256
	global_load_dwordx4 v[14:17], v[182:183], off
	global_load_dwordx4 v[10:13], v[182:183], off offset:256
	global_load_dwordx4 v[6:9], v[178:179], off
	global_load_dwordx4 v[2:5], v[178:179], off offset:256
	v_mov_b32_e32 v242, 0x40000
	v_mov_b32_e32 v243, 0
	v_lshl_add_u64 v[240:241], v[190:191], 0, v[242:243]
	global_load_dwordx4 v[208:211], v[240:241], off
	global_load_dwordx4 v[212:215], v[240:241], off offset:256
	v_lshl_add_u64 v[240:241], v[186:187], 0, v[242:243]
	global_load_dwordx4 v[216:219], v[240:241], off
	global_load_dwordx4 v[220:223], v[240:241], off offset:256
	v_lshl_add_u64 v[240:241], v[182:183], 0, v[242:243]
	global_load_dwordx4 v[224:227], v[240:241], off
	global_load_dwordx4 v[228:231], v[240:241], off offset:256
	v_lshl_add_u64 v[240:241], v[178:179], 0, v[242:243]
	global_load_dwordx4 v[232:235], v[240:241], off
	global_load_dwordx4 v[236:239], v[240:241], off offset:256
	v_lshlrev_b64 v[188:189], 10, v[32:33]
	v_lshl_add_u64 v[188:189], v[30:31], 0, v[188:189]
	s_lshl_b32 s26, s60, 2
	s_ashr_i32 s27, s26, 31
	s_lshl_b64 s[26:27], s[26:27], 2
	s_add_u32 s26, s49, s26
	s_addc_u32 s27, s50, s27
	s_waitcnt vmcnt(8)
	v_lshlrev_b32_e32 v196, 16, v204
	v_and_b32_e32 v197, 0xffff0000, v204
	v_lshlrev_b32_e32 v198, 16, v205
	v_and_b32_e32 v199, 0xffff0000, v205
	v_pk_add_f32 v[160:161], v[160:161], v[198:199]
	v_pk_add_f32 v[196:197], v[158:159], v[196:197]
	v_lshlrev_b32_e32 v158, 16, v206
	v_and_b32_e32 v159, 0xffff0000, v206
	v_lshlrev_b32_e32 v198, 16, v207
	v_and_b32_e32 v199, 0xffff0000, v207
	v_pk_add_f32 v[154:155], v[154:155], v[158:159]
	v_mul_f32_e32 v158, v197, v197
	v_mul_f32_e32 v159, v161, v161
	v_pk_add_f32 v[156:157], v[156:157], v[198:199]
	v_fmac_f32_e32 v158, v196, v196
	v_fmac_f32_e32 v159, v160, v160
	v_add_f32_e32 v158, v158, v159
	v_mul_f32_e32 v159, v155, v155
	v_mul_f32_e32 v195, v157, v157
	v_fmac_f32_e32 v159, v154, v154
	v_fmac_f32_e32 v195, v156, v156
	v_cvt_pk_bf16_f32 v204, v196, v197
	v_cvt_pk_bf16_f32 v205, v160, v161
	v_cvt_pk_bf16_f32 v206, v154, v155
	v_mul_f32_e32 v154, 0x41000000, v154
	v_mul_f32_e32 v155, 0x41000000, v155
	v_add_f32_e32 v159, v159, v195
	v_mul_f32_e32 v195, 0x41000000, v197
	v_med3_f32 v154, v154, s64, v250
	v_med3_f32 v155, v155, s64, v250
	v_mov_b32_e32 v197, v1
	v_cvt_pk_fp8_f32 v197, v154, v155
	v_add_f32_e32 v158, v158, v159
	v_mul_f32_e32 v159, 0x41000000, v196
	v_mul_f32_e32 v154, 0x41000000, v156
	v_mul_f32_e32 v155, 0x41000000, v157
	v_med3_f32 v159, v159, s64, v250
	v_med3_f32 v195, v195, s64, v250
	v_mov_b32_e32 v196, v1
	v_med3_f32 v154, v154, s64, v250
	v_med3_f32 v155, v155, s64, v250
	v_cvt_pk_fp8_f32 v196, v159, v195
	v_cvt_pk_fp8_f32 v197, v154, v155 op_sel:[0,0,1]
	v_lshlrev_b32_e32 v154, 16, v26
	v_and_b32_e32 v155, 0xffff0000, v26
	v_lshlrev_b32_e32 v26, 16, v27
	v_and_b32_e32 v27, 0xffff0000, v27
	v_pk_add_f32 v[26:27], v[152:153], v[26:27]
	v_pk_add_f32 v[150:151], v[150:151], v[154:155]
	v_lshlrev_b32_e32 v152, 16, v28
	v_and_b32_e32 v153, 0xffff0000, v28
	v_mul_f32_e32 v159, 0x41000000, v160
	v_mul_f32_e32 v160, 0x41000000, v161
	v_lshlrev_b32_e32 v28, 16, v29
	v_and_b32_e32 v29, 0xffff0000, v29
	v_pk_add_f32 v[152:153], v[146:147], v[152:153]
	v_mul_f32_e32 v146, v151, v151
	v_mul_f32_e32 v147, v27, v27
	v_med3_f32 v159, v159, s64, v250
	v_med3_f32 v160, v160, s64, v250
	v_pk_add_f32 v[28:29], v[148:149], v[28:29]
	v_fmac_f32_e32 v146, v150, v150
	v_fmac_f32_e32 v147, v26, v26
	v_cvt_pk_fp8_f32 v196, v159, v160 op_sel:[0,0,1]
	v_add_f32_e32 v146, v146, v147
	v_mul_f32_e32 v147, v153, v153
	v_mul_f32_e32 v148, v29, v29
	v_fmac_f32_e32 v147, v152, v152
	v_fmac_f32_e32 v148, v28, v28
	v_add_f32_e32 v147, v147, v148
	v_add_f32_e32 v146, v146, v147
	v_cvt_pk_bf16_f32 v207, v156, v157
	global_store_dwordx4 v[190:191], v[204:207], off
	global_store_dwordx2 v[188:189], v[196:197], off
	v_add_f32_e32 v154, v158, v146
	v_cvt_pk_bf16_f32 v146, v150, v151
	v_cvt_pk_bf16_f32 v147, v26, v27
	v_cvt_pk_bf16_f32 v148, v152, v153
	v_cvt_pk_bf16_f32 v149, v28, v29
	global_store_dwordx4 v[190:191], v[146:149], off offset:256
	v_mul_f32_e32 v26, 0x41000000, v26
	v_mul_f32_e32 v27, 0x41000000, v27
	v_mul_f32_e32 v146, 0x41000000, v150
	v_med3_f32 v147, v146, s64, v250
	v_mul_f32_e32 v146, 0x41000000, v151
	v_med3_f32 v148, v146, s64, v250
	v_mov_b32_e32 v146, v1
	v_cvt_pk_fp8_f32 v146, v147, v148
	v_med3_f32 v26, v26, s64, v250
	v_med3_f32 v27, v27, s64, v250
	v_mov_b32_e32 v147, v1
	v_cvt_pk_fp8_f32 v146, v26, v27 op_sel:[0,0,1]
	v_mul_f32_e32 v26, 0x41000000, v152
	v_mul_f32_e32 v27, 0x41000000, v153
	v_med3_f32 v26, v26, s64, v250
	v_med3_f32 v27, v27, s64, v250
	v_cvt_pk_fp8_f32 v147, v26, v27
	v_mul_f32_e32 v26, 0x41000000, v28
	v_mul_f32_e32 v27, 0x41000000, v29
	v_med3_f32 v26, v26, s64, v250
	v_med3_f32 v27, v27, s64, v250
	v_cvt_pk_fp8_f32 v147, v26, v27 op_sel:[0,0,1]
	ds_swizzle_b32 v26, v154 offset:swizzle(SWAP,16)
	global_store_dwordx2 v[188:189], v[146:147], off offset:128
	s_waitcnt lgkmcnt(0)
	v_add_f32_e32 v26, v154, v26
	v_mov_b32_e32 v27, v26
	s_nop 1
	v_permlane32_swap_b32_e32 v26, v27
	s_and_saveexec_b64 s[28:29], s[2:3]
	s_cbranch_execz .LBB0_1863
	v_lshlrev_b64 v[28:29], 6, v[32:33]
	v_lshl_add_u64 v[28:29], s[26:27], 0, v[28:29]
	v_add_f32_e32 v26, v26, v27
	global_store_dword v[28:29], v26, off

; __device__ __forceinline__ u32x4 pack8(const f32x4 a, const f32x4 b) { u32x4 w; w.x = cvt_pk_bf16(a[0], a[1]); w.y = cvt_pk_bf16(a[2], a[3]); w.z = cvt_pk_bf16(b[0], b[1]); w.w = cvt_pk_bf16(b[2], b[3]); return w; }
; __device__ __forceinline__ float sumsq4(const f32x4 v) { return (v[0] * v[0] + v[1] * v[1]) + (v[2] * v[2] + v[3] * v[3]); }
; __device__ __forceinline__ float xor16_add(float v) { return v + __int_as_float(__builtin_amdgcn_ds_swizzle(__float_as_int(v), 0x401F)); }
; __device__ __forceinline__ float xor32_add(float v) { auto rr = __builtin_amdgcn_permlane32_swap(__float_as_uint(v), __float_as_uint(v), false, false); return __uint_as_float(rr[0]) + __uint_as_float(rr[1]); }
; __device__ __forceinline__ f32x4 bf2f_lo(const u32x4 w, int h) { const unsigned a = h ? w.z : w.x, b = h ? w.w : w.y; return (f32x4){__uint_as_float(a << 16), __uint_as_float(a & 0xffff0000u), __uint_as_float(b << 16), __uint_as_float(b & 0xffff0000u)}; }
;     __device__ __forceinline__ void operator()(const f32x4 (&acc)[2][2][4][2], const Unit& u, int wr, int wc, int fr, int fq) const {
;     ...
;                 for (int bj = 0; bj < 2; ++bj) old[m][bj] = *(const u32x4*)(xb + (size_t)(row0 + ai * HALF + m * 16) * DM + col0 + bj * HALF);
; #pragma unroll
;             for (int m = 0; m < 4; ++m) {
;                 const int row = row0 + ai * HALF + m * 16; float ss = 0.f;
; #pragma unroll
;                 for (int bj = 0; bj < 2; ++bj) {
;                     const f32x4 v0 = bf2f_lo(old[m][bj], 0) + acc[ai][bj][m][0], v1 = bf2f_lo(old[m][bj], 1) + acc[ai][bj][m][1];
;                     ss += sumsq4(v0) + sumsq4(v1);
;                     *(u32x4*)(xb + (size_t)row * DM + col0 + bj * HALF) = pack8(v0, v1);
;                     { u32x2 w8; w8.x = pack4_fp8_x8(v0); w8.y = pack4_fp8_x8(v1); *(u32x2*)(xq + (size_t)row * DM + col0 + bj * HALF) = w8; }
;                 }
;                 ss = xor32_add(xor16_add(ss));
;                 if (fq == 0) ssx[(size_t)row * 16 + u.pn * 4 + wc] = ss;
.LBB0_1869:
	s_or_b64 exec, exec, s[28:29]
	v_add_u32_e32 v108, 0x80, v32
	v_ashrrev_i32_e32 v109, 31, v108
	v_lshlrev_b64 v[2:3], 11, v[108:109]
	v_lshl_add_u64 v[110:111], v[174:175], 0, v[2:3]
	v_add_u32_e32 v104, 0x90, v32
	v_ashrrev_i32_e32 v105, 31, v104
	v_add_u32_e32 v100, 0xa0, v32
	v_lshlrev_b64 v[2:3], 11, v[104:105]
	v_ashrrev_i32_e32 v101, 31, v100
	v_add_u32_e32 v32, 0xb0, v32
	v_lshl_add_u64 v[106:107], v[174:175], 0, v[2:3]
	v_lshlrev_b64 v[2:3], 11, v[100:101]
	v_ashrrev_i32_e32 v33, 31, v32
	v_lshl_add_u64 v[102:103], v[174:175], 0, v[2:3]
	v_lshlrev_b64 v[2:3], 11, v[32:33]
	v_lshl_add_u64 v[98:99], v[174:175], 0, v[2:3]
	s_waitcnt vmcnt(16)
	v_mov_b32_e32 v114, v208
	v_mov_b32_e32 v115, v209
	v_mov_b32_e32 v116, v210
	v_mov_b32_e32 v117, v211
	v_mov_b32_e32 v26, v212
	v_mov_b32_e32 v27, v213
	v_mov_b32_e32 v28, v214
	v_mov_b32_e32 v29, v215
	v_mov_b32_e32 v22, v216
	v_mov_b32_e32 v23, v217
	v_mov_b32_e32 v24, v218
	v_mov_b32_e32 v25, v219
	v_mov_b32_e32 v18, v220
	v_mov_b32_e32 v19, v221
	v_mov_b32_e32 v20, v222
	v_mov_b32_e32 v21, v223
	v_mov_b32_e32 v14, v224
	v_mov_b32_e32 v15, v225
	v_mov_b32_e32 v16, v226
	v_mov_b32_e32 v17, v227
	v_mov_b32_e32 v10, v228
	v_mov_b32_e32 v11, v229
	v_mov_b32_e32 v12, v230
	v_mov_b32_e32 v13, v231
	v_mov_b32_e32 v6, v232
	v_mov_b32_e32 v7, v233
	v_mov_b32_e32 v8, v234
	v_mov_b32_e32 v9, v235
	v_mov_b32_e32 v2, v236
	v_mov_b32_e32 v3, v237
	v_mov_b32_e32 v4, v238
	v_mov_b32_e32 v5, v239
	v_lshlrev_b64 v[112:113], 10, v[108:109]
	v_lshl_add_u64 v[112:113], v[30:31], 0, v[112:113]
	v_lshlrev_b32_e32 v118, 16, v114
	v_and_b32_e32 v119, 0xffff0000, v114
	v_lshlrev_b32_e32 v114, 16, v115
	v_and_b32_e32 v115, 0xffff0000, v115
	v_pk_add_f32 v[114:115], v[96:97], v[114:115]
	v_pk_add_f32 v[118:119], v[94:95], v[118:119]
	v_lshlrev_b32_e32 v94, 16, v116
	v_and_b32_e32 v95, 0xffff0000, v116
	v_lshlrev_b32_e32 v96, 16, v117
	v_and_b32_e32 v97, 0xffff0000, v117
	v_pk_add_f32 v[116:117], v[90:91], v[94:95]
	v_mul_f32_e32 v90, v119, v119
	v_mul_f32_e32 v91, v115, v115
	v_pk_add_f32 v[92:93], v[92:93], v[96:97]
	v_fmac_f32_e32 v90, v118, v118
	v_fmac_f32_e32 v91, v114, v114
	v_add_f32_e32 v90, v90, v91
	v_mul_f32_e32 v91, v117, v117
	v_mul_f32_e32 v94, v93, v93
	v_fmac_f32_e32 v91, v116, v116
	v_fmac_f32_e32 v94, v92, v92
	v_add_f32_e32 v91, v91, v94
	v_cvt_pk_bf16_f32 v94, v118, v119
	v_add_f32_e32 v90, v90, v91
	v_cvt_pk_bf16_f32 v95, v114, v115
	v_cvt_pk_bf16_f32 v96, v116, v117
	v_cvt_pk_bf16_f32 v97, v92, v93
	global_store_dwordx4 v[110:111], v[94:97], off
	v_mul_f32_e32 v91, 0x41000000, v118
	v_med3_f32 v91, v91, s64, v250
	v_mul_f32_e32 v94, 0x41000000, v119
	v_med3_f32 v95, v94, s64, v250
	v_mov_b32_e32 v94, v1
	v_cvt_pk_fp8_f32 v94, v91, v95
	v_mul_f32_e32 v91, 0x41000000, v114
	v_mul_f32_e32 v95, 0x41000000, v115
	v_med3_f32 v91, v91, s64, v250
	v_med3_f32 v95, v95, s64, v250
	v_cvt_pk_fp8_f32 v94, v91, v95 op_sel:[0,0,1]
	v_mul_f32_e32 v91, 0x41000000, v116
	v_mul_f32_e32 v95, 0x41000000, v117
	v_med3_f32 v91, v91, s64, v250
	v_med3_f32 v96, v95, s64, v250
	v_mov_b32_e32 v95, v1
	v_cvt_pk_fp8_f32 v95, v91, v96
	v_mul_f32_e32 v91, 0x41000000, v92
	v_mul_f32_e32 v92, 0x41000000, v93
	v_med3_f32 v91, v91, s64, v250
	v_med3_f32 v92, v92, s64, v250
	v_cvt_pk_fp8_f32 v95, v91, v92 op_sel:[0,0,1]
	v_lshlrev_b32_e32 v92, 16, v26
	v_and_b32_e32 v93, 0xffff0000, v26
	v_lshlrev_b32_e32 v26, 16, v27
	v_and_b32_e32 v27, 0xffff0000, v27
	v_pk_add_f32 v[26:27], v[88:89], v[26:27]
	v_pk_add_f32 v[86:87], v[86:87], v[92:93]
	v_lshlrev_b32_e32 v88, 16, v28
	v_and_b32_e32 v89, 0xffff0000, v28
	v_lshlrev_b32_e32 v28, 16, v29
	v_and_b32_e32 v29, 0xffff0000, v29
	v_pk_add_f32 v[88:89], v[82:83], v[88:89]
	v_mul_f32_e32 v82, v87, v87
	v_mul_f32_e32 v83, v27, v27
	v_pk_add_f32 v[28:29], v[84:85], v[28:29]
	v_fmac_f32_e32 v82, v86, v86
	v_fmac_f32_e32 v83, v26, v26
	v_add_f32_e32 v82, v82, v83
	v_mul_f32_e32 v83, v89, v89
	v_mul_f32_e32 v84, v29, v29
	v_fmac_f32_e32 v83, v88, v88
	v_fmac_f32_e32 v84, v28, v28
	v_add_f32_e32 v83, v83, v84
	v_add_f32_e32 v82, v82, v83
	global_store_dwordx2 v[112:113], v[94:95], off
	v_add_f32_e32 v90, v90, v82
	v_cvt_pk_bf16_f32 v82, v86, v87
	v_cvt_pk_bf16_f32 v83, v26, v27
	v_cvt_pk_bf16_f32 v84, v88, v89
	v_cvt_pk_bf16_f32 v85, v28, v29
	global_store_dwordx4 v[110:111], v[82:85], off offset:256
	v_mul_f32_e32 v26, 0x41000000, v26
	v_mul_f32_e32 v27, 0x41000000, v27
	v_mul_f32_e32 v82, 0x41000000, v86
	v_med3_f32 v83, v82, s64, v250
	v_mul_f32_e32 v82, 0x41000000, v87
	v_med3_f32 v84, v82, s64, v250
	v_mov_b32_e32 v82, v1
	v_cvt_pk_fp8_f32 v82, v83, v84
	v_med3_f32 v26, v26, s64, v250
	v_med3_f32 v27, v27, s64, v250
	v_mov_b32_e32 v83, v1
	v_cvt_pk_fp8_f32 v82, v26, v27 op_sel:[0,0,1]
	v_mul_f32_e32 v26, 0x41000000, v88
	v_mul_f32_e32 v27, 0x41000000, v89
	v_med3_f32 v26, v26, s64, v250
	v_med3_f32 v27, v27, s64, v250
	v_cvt_pk_fp8_f32 v83, v26, v27
	v_mul_f32_e32 v26, 0x41000000, v28
	v_mul_f32_e32 v27, 0x41000000, v29
	v_med3_f32 v26, v26, s64, v250
	v_med3_f32 v27, v27, s64, v250
	v_cvt_pk_fp8_f32 v83, v26, v27 op_sel:[0,0,1]
	ds_swizzle_b32 v26, v90 offset:swizzle(SWAP,16)
	global_store_dwordx2 v[112:113], v[82:83], off offset:128
	s_waitcnt lgkmcnt(0)
	v_add_f32_e32 v26, v90, v26
	v_mov_b32_e32 v27, v26
	s_nop 1
	v_permlane32_swap_b32_e32 v26, v27
	s_and_saveexec_b64 s[28:29], s[2:3]
	s_cbranch_execz .LBB0_1871
	v_lshlrev_b64 v[28:29], 6, v[108:109]
	v_lshl_add_u64 v[28:29], s[26:27], 0, v[28:29]
	v_add_f32_e32 v26, v26, v27
	global_store_dword v[28:29], v26, off
; __device__ __forceinline__ u32x4 pack8(const f32x4 a, const f32x4 b) { u32x4 w; w.x = cvt_pk_bf16(a[0], a[1]); w.y = cvt_pk_bf16(a[2], a[3]); w.z = cvt_pk_bf16(b[0], b[1]); w.w = cvt_pk_bf16(b[2], b[3]); return w; }
; __device__ __forceinline__ float sumsq4(const f32x4 v) { return (v[0] * v[0] + v[1] * v[1]) + (v[2] * v[2] + v[3] * v[3]); }
; __device__ __forceinline__ float xor16_add(float v) { return v + __int_as_float(__builtin_amdgcn_ds_swizzle(__float_as_int(v), 0x401F)); }
; __device__ __forceinline__ float xor32_add(float v) { auto rr = __builtin_amdgcn_permlane32_swap(__float_as_uint(v), __float_as_uint(v), false, false); return __uint_as_float(rr[0]) + __uint_as_float(rr[1]); }
; __device__ __forceinline__ f32x4 bf2f_lo(const u32x4 w, int h) { const unsigned a = h ? w.z : w.x, b = h ? w.w : w.y; return (f32x4){__uint_as_float(a << 16), __uint_as_float(a & 0xffff0000u), __uint_as_float(b << 16), __uint_as_float(b & 0xffff0000u)}; }
;     __device__ __forceinline__ void operator()(const f32x4 (&acc)[2][2][4][2], const Unit& u, int wr, int wc, int fr, int fq) const {
;     ...
;             for (int m = 0; m < 4; ++m) {
;                 const int row = row0 + ai * HALF + m * 16; float ss = 0.f;
; #pragma unroll
;                 for (int bj = 0; bj < 2; ++bj) {
;                     const f32x4 v0 = bf2f_lo(old[m][bj], 0) + acc[ai][bj][m][0], v1 = bf2f_lo(old[m][bj], 1) + acc[ai][bj][m][1];
;                     ss += sumsq4(v0) + sumsq4(v1);
;                     *(u32x4*)(xb + (size_t)row * DM + col0 + bj * HALF) = pack8(v0, v1);
;                     { u32x2 w8; w8.x = pack4_fp8_x8(v0); w8.y = pack4_fp8_x8(v1); *(u32x2*)(xq + (size_t)row * DM + col0 + bj * HALF) = w8; }
;                 }
;                 ss = xor32_add(xor16_add(ss));
;                 if (fq == 0) ssx[(size_t)row * 16 + u.pn * 4 + wc] = ss;
.LBB0_1871:
	s_or_b64 exec, exec, s[28:29]
	v_lshlrev_b32_e32 v28, 16, v22
	v_and_b32_e32 v29, 0xffff0000, v22
	v_lshlrev_b32_e32 v22, 16, v23
	v_and_b32_e32 v23, 0xffff0000, v23
	v_pk_add_f32 v[80:81], v[80:81], v[22:23]
	v_pk_add_f32 v[28:29], v[78:79], v[28:29]
	v_lshlrev_b32_e32 v22, 16, v24
	v_and_b32_e32 v23, 0xffff0000, v24
	v_lshlrev_b32_e32 v24, 16, v25
	v_and_b32_e32 v25, 0xffff0000, v25
	v_pk_add_f32 v[76:77], v[76:77], v[24:25]
	v_pk_add_f32 v[24:25], v[74:75], v[22:23]
	v_mul_f32_e32 v22, v29, v29
	v_mul_f32_e32 v23, v81, v81
	v_fmac_f32_e32 v22, v28, v28
	v_fmac_f32_e32 v23, v80, v80
	v_add_f32_e32 v22, v22, v23
	v_mul_f32_e32 v23, v25, v25
	v_mul_f32_e32 v74, v77, v77
	v_fmac_f32_e32 v23, v24, v24
	v_fmac_f32_e32 v74, v76, v76
	v_add_f32_e32 v23, v23, v74
	v_add_f32_e32 v74, v22, v23
	v_cvt_pk_bf16_f32 v22, v28, v29
	v_mul_f32_e32 v28, 0x41000000, v28
	v_med3_f32 v75, v28, s64, v250
	v_mul_f32_e32 v28, 0x41000000, v29
	v_med3_f32 v29, v28, s64, v250
	v_mov_b32_e32 v28, v1
	v_cvt_pk_fp8_f32 v28, v75, v29
	v_mul_f32_e32 v29, 0x41000000, v80
	v_mul_f32_e32 v75, 0x41000000, v81
	v_med3_f32 v29, v29, s64, v250
	v_med3_f32 v75, v75, s64, v250
	v_cvt_pk_fp8_f32 v28, v29, v75 op_sel:[0,0,1]
	v_mul_f32_e32 v29, 0x41000000, v24
	v_med3_f32 v75, v29, s64, v250
	v_mul_f32_e32 v29, 0x41000000, v25
	v_med3_f32 v78, v29, s64, v250
	v_mov_b32_e32 v29, v1
	v_cvt_pk_fp8_f32 v29, v75, v78
	v_mul_f32_e32 v75, 0x41000000, v76
	v_mul_f32_e32 v78, 0x41000000, v77
	v_med3_f32 v75, v75, s64, v250
	v_med3_f32 v78, v78, s64, v250
	v_cvt_pk_fp8_f32 v29, v75, v78 op_sel:[0,0,1]
	v_lshlrev_b64 v[26:27], 10, v[104:105]
	v_cvt_pk_bf16_f32 v23, v80, v81
	v_cvt_pk_bf16_f32 v24, v24, v25
	v_cvt_pk_bf16_f32 v25, v76, v77
	v_lshl_add_u64 v[26:27], v[30:31], 0, v[26:27]
	global_store_dwordx4 v[106:107], v[22:25], off
	global_store_dwordx2 v[26:27], v[28:29], off
	v_lshlrev_b32_e32 v22, 16, v18
	v_and_b32_e32 v23, 0xffff0000, v18
	v_lshlrev_b32_e32 v18, 16, v19
	v_and_b32_e32 v19, 0xffff0000, v19
	v_pk_add_f32 v[24:25], v[72:73], v[18:19]
	v_pk_add_f32 v[22:23], v[70:71], v[22:23]
	v_lshlrev_b32_e32 v18, 16, v20
	v_and_b32_e32 v19, 0xffff0000, v20
	v_lshlrev_b32_e32 v20, 16, v21
	v_and_b32_e32 v21, 0xffff0000, v21
	v_pk_add_f32 v[28:29], v[68:69], v[20:21]
	v_pk_add_f32 v[20:21], v[66:67], v[18:19]
	v_mul_f32_e32 v18, v23, v23
	v_mul_f32_e32 v19, v25, v25
	v_fmac_f32_e32 v18, v22, v22
	v_fmac_f32_e32 v19, v24, v24
	v_add_f32_e32 v18, v18, v19
	v_mul_f32_e32 v19, v21, v21
	v_mul_f32_e32 v66, v29, v29
	v_fmac_f32_e32 v19, v20, v20
	v_fmac_f32_e32 v66, v28, v28
	v_add_f32_e32 v19, v19, v66
	v_add_f32_e32 v18, v18, v19
	v_add_f32_e32 v66, v74, v18
	v_cvt_pk_bf16_f32 v18, v22, v23
	v_mul_f32_e32 v22, 0x41000000, v22
	v_med3_f32 v67, v22, s64, v250
	v_mul_f32_e32 v22, 0x41000000, v23
	v_med3_f32 v23, v22, s64, v250
	v_mov_b32_e32 v22, v1
	v_cvt_pk_fp8_f32 v22, v67, v23
	v_cvt_pk_bf16_f32 v19, v24, v25
	v_mul_f32_e32 v23, 0x41000000, v24
	v_mul_f32_e32 v24, 0x41000000, v25
	v_med3_f32 v23, v23, s64, v250
	v_med3_f32 v24, v24, s64, v250
	v_cvt_pk_fp8_f32 v22, v23, v24 op_sel:[0,0,1]
	v_mul_f32_e32 v23, 0x41000000, v20
	v_med3_f32 v24, v23, s64, v250
	v_mul_f32_e32 v23, 0x41000000, v21
	v_med3_f32 v25, v23, s64, v250
	v_mov_b32_e32 v23, v1
	v_cvt_pk_fp8_f32 v23, v24, v25
	v_mul_f32_e32 v24, 0x41000000, v28
	v_mul_f32_e32 v25, 0x41000000, v29
	v_med3_f32 v24, v24, s64, v250
	v_med3_f32 v25, v25, s64, v250
	v_cvt_pk_fp8_f32 v23, v24, v25 op_sel:[0,0,1]
	ds_swizzle_b32 v24, v66 offset:swizzle(SWAP,16)
	v_cvt_pk_bf16_f32 v20, v20, v21
	v_cvt_pk_bf16_f32 v21, v28, v29
	global_store_dwordx4 v[106:107], v[18:21], off offset:256
	global_store_dwordx2 v[26:27], v[22:23], off offset:128
	s_waitcnt lgkmcnt(0)
	v_add_f32_e32 v18, v66, v24
	v_mov_b32_e32 v19, v18
	s_nop 1
	v_permlane32_swap_b32_e32 v18, v19
	s_and_saveexec_b64 s[28:29], s[2:3]
	s_cbranch_execz .LBB0_1873
	v_lshlrev_b64 v[20:21], 6, v[104:105]
	v_lshl_add_u64 v[20:21], s[26:27], 0, v[20:21]
	v_add_f32_e32 v18, v18, v19
	global_store_dword v[20:21], v18, off
.LBB0_1873:
	s_or_b64 exec, exec, s[28:29]
	v_lshlrev_b32_e32 v20, 16, v14
	v_and_b32_e32 v21, 0xffff0000, v14
	v_lshlrev_b32_e32 v14, 16, v15
	v_and_b32_e32 v15, 0xffff0000, v15
	v_pk_add_f32 v[22:23], v[64:65], v[14:15]
	v_pk_add_f32 v[20:21], v[62:63], v[20:21]
	v_lshlrev_b32_e32 v14, 16, v16
	v_and_b32_e32 v15, 0xffff0000, v16
	v_lshlrev_b32_e32 v16, 16, v17
	v_and_b32_e32 v17, 0xffff0000, v17
	v_pk_add_f32 v[24:25], v[60:61], v[16:17]
	v_pk_add_f32 v[16:17], v[58:59], v[14:15]
	v_mul_f32_e32 v14, v21, v21
	v_mul_f32_e32 v15, v23, v23
	v_fmac_f32_e32 v14, v20, v20
	v_fmac_f32_e32 v15, v22, v22
	v_add_f32_e32 v14, v14, v15
	v_mul_f32_e32 v15, v17, v17
	v_mul_f32_e32 v26, v25, v25
	v_fmac_f32_e32 v15, v16, v16
	v_fmac_f32_e32 v26, v24, v24
	v_add_f32_e32 v15, v15, v26
	v_add_f32_e32 v26, v14, v15
	v_cvt_pk_bf16_f32 v14, v20, v21
	v_mul_f32_e32 v20, 0x41000000, v20
	v_med3_f32 v27, v20, s64, v250
	v_mul_f32_e32 v20, 0x41000000, v21
	v_med3_f32 v21, v20, s64, v250
	v_mov_b32_e32 v20, v1
	v_cvt_pk_fp8_f32 v20, v27, v21
	v_cvt_pk_bf16_f32 v15, v22, v23
	v_mul_f32_e32 v21, 0x41000000, v22
	v_mul_f32_e32 v22, 0x41000000, v23
	v_med3_f32 v21, v21, s64, v250
	v_med3_f32 v22, v22, s64, v250
	v_cvt_pk_fp8_f32 v20, v21, v22 op_sel:[0,0,1]
	v_mul_f32_e32 v21, 0x41000000, v16
	v_med3_f32 v22, v21, s64, v250
	v_mul_f32_e32 v21, 0x41000000, v17
	v_med3_f32 v23, v21, s64, v250
	v_mov_b32_e32 v21, v1
	v_cvt_pk_fp8_f32 v21, v22, v23
	v_mul_f32_e32 v22, 0x41000000, v24
	v_mul_f32_e32 v23, 0x41000000, v25
	v_med3_f32 v22, v22, s64, v250
	v_med3_f32 v23, v23, s64, v250
; __device__ __forceinline__ u32x4 pack8(const f32x4 a, const f32x4 b) { u32x4 w; w.x = cvt_pk_bf16(a[0], a[1]); w.y = cvt_pk_bf16(a[2], a[3]); w.z = cvt_pk_bf16(b[0], b[1]); w.w = cvt_pk_bf16(b[2], b[3]); return w; }
; __device__ __forceinline__ float sumsq4(const f32x4 v) { return (v[0] * v[0] + v[1] * v[1]) + (v[2] * v[2] + v[3] * v[3]); }
; __device__ __forceinline__ float xor16_add(float v) { return v + __int_as_float(__builtin_amdgcn_ds_swizzle(__float_as_int(v), 0x401F)); }
; __device__ __forceinline__ float xor32_add(float v) { auto rr = __builtin_amdgcn_permlane32_swap(__float_as_uint(v), __float_as_uint(v), false, false); return __uint_as_float(rr[0]) + __uint_as_float(rr[1]); }
; __device__ __forceinline__ f32x4 bf2f_lo(const u32x4 w, int h) { const unsigned a = h ? w.z : w.x, b = h ? w.w : w.y; return (f32x4){__uint_as_float(a << 16), __uint_as_float(a & 0xffff0000u), __uint_as_float(b << 16), __uint_as_float(b & 0xffff0000u)}; }
;     __device__ __forceinline__ void operator()(const f32x4 (&acc)[2][2][4][2], const Unit& u, int wr, int wc, int fr, int fq) const {
;     ...
;             for (int m = 0; m < 4; ++m) {
;                 const int row = row0 + ai * HALF + m * 16; float ss = 0.f;
; #pragma unroll
;                 for (int bj = 0; bj < 2; ++bj) {
;                     const f32x4 v0 = bf2f_lo(old[m][bj], 0) + acc[ai][bj][m][0], v1 = bf2f_lo(old[m][bj], 1) + acc[ai][bj][m][1];
;                     ss += sumsq4(v0) + sumsq4(v1);
;                     *(u32x4*)(xb + (size_t)row * DM + col0 + bj * HALF) = pack8(v0, v1);
;                     { u32x2 w8; w8.x = pack4_fp8_x8(v0); w8.y = pack4_fp8_x8(v1); *(u32x2*)(xq + (size_t)row * DM + col0 + bj * HALF) = w8; }
;                 }
;                 ss = xor32_add(xor16_add(ss));
;                 if (fq == 0) ssx[(size_t)row * 16 + u.pn * 4 + wc] = ss;
	v_cvt_pk_fp8_f32 v21, v22, v23 op_sel:[0,0,1]
	v_lshlrev_b64 v[18:19], 10, v[100:101]
	v_cvt_pk_bf16_f32 v16, v16, v17
	v_cvt_pk_bf16_f32 v17, v24, v25
	v_lshl_add_u64 v[18:19], v[30:31], 0, v[18:19]
	global_store_dwordx4 v[102:103], v[14:17], off
	global_store_dwordx2 v[18:19], v[20:21], off
	v_lshlrev_b32_e32 v14, 16, v10
	v_and_b32_e32 v15, 0xffff0000, v10
	v_lshlrev_b32_e32 v10, 16, v11
	v_and_b32_e32 v11, 0xffff0000, v11
	v_pk_add_f32 v[16:17], v[56:57], v[10:11]
	v_pk_add_f32 v[14:15], v[54:55], v[14:15]
	v_lshlrev_b32_e32 v10, 16, v12
	v_and_b32_e32 v11, 0xffff0000, v12
	v_lshlrev_b32_e32 v12, 16, v13
	v_and_b32_e32 v13, 0xffff0000, v13
	v_pk_add_f32 v[20:21], v[52:53], v[12:13]
	v_pk_add_f32 v[12:13], v[50:51], v[10:11]
	v_mul_f32_e32 v10, v15, v15
	v_mul_f32_e32 v11, v17, v17
	v_fmac_f32_e32 v10, v14, v14
	v_fmac_f32_e32 v11, v16, v16
	v_add_f32_e32 v10, v10, v11
	v_mul_f32_e32 v11, v13, v13
	v_mul_f32_e32 v22, v21, v21
	v_fmac_f32_e32 v11, v12, v12
	v_fmac_f32_e32 v22, v20, v20
	v_add_f32_e32 v11, v11, v22
	v_add_f32_e32 v10, v10, v11
	v_add_f32_e32 v22, v26, v10
	v_cvt_pk_bf16_f32 v10, v14, v15
	v_mul_f32_e32 v14, 0x41000000, v14
	v_med3_f32 v23, v14, s64, v250
	v_mul_f32_e32 v14, 0x41000000, v15
	v_med3_f32 v15, v14, s64, v250
	v_mov_b32_e32 v14, v1
	v_cvt_pk_fp8_f32 v14, v23, v15
	v_cvt_pk_bf16_f32 v11, v16, v17
	v_mul_f32_e32 v15, 0x41000000, v16
	v_mul_f32_e32 v16, 0x41000000, v17
	v_med3_f32 v15, v15, s64, v250
	v_med3_f32 v16, v16, s64, v250
	v_cvt_pk_fp8_f32 v14, v15, v16 op_sel:[0,0,1]
	v_mul_f32_e32 v15, 0x41000000, v12
	v_med3_f32 v16, v15, s64, v250
	v_mul_f32_e32 v15, 0x41000000, v13
	v_med3_f32 v17, v15, s64, v250
	v_mov_b32_e32 v15, v1
	v_cvt_pk_fp8_f32 v15, v16, v17
	v_mul_f32_e32 v16, 0x41000000, v20
	v_mul_f32_e32 v17, 0x41000000, v21
	v_med3_f32 v16, v16, s64, v250
	v_med3_f32 v17, v17, s64, v250
	v_cvt_pk_fp8_f32 v15, v16, v17 op_sel:[0,0,1]
	ds_swizzle_b32 v16, v22 offset:swizzle(SWAP,16)
	v_cvt_pk_bf16_f32 v12, v12, v13
	v_cvt_pk_bf16_f32 v13, v20, v21
	global_store_dwordx4 v[102:103], v[10:13], off offset:256
	global_store_dwordx2 v[18:19], v[14:15], off offset:128
	s_waitcnt lgkmcnt(0)
	v_add_f32_e32 v10, v22, v16
	v_mov_b32_e32 v11, v10
	s_nop 1
	v_permlane32_swap_b32_e32 v10, v11
	s_and_saveexec_b64 s[28:29], s[2:3]
	s_cbranch_execz .LBB0_1875
	v_lshlrev_b64 v[12:13], 6, v[100:101]
	v_lshl_add_u64 v[12:13], s[26:27], 0, v[12:13]
	v_add_f32_e32 v10, v10, v11
	global_store_dword v[12:13], v10, off
.LBB0_1875:
	s_or_b64 exec, exec, s[28:29]
	v_lshlrev_b32_e32 v12, 16, v6
	v_and_b32_e32 v13, 0xffff0000, v6
	v_lshlrev_b32_e32 v6, 16, v7
	v_and_b32_e32 v7, 0xffff0000, v7
	v_pk_add_f32 v[14:15], v[48:49], v[6:7]
	v_pk_add_f32 v[12:13], v[46:47], v[12:13]
	v_lshlrev_b32_e32 v6, 16, v8
	v_and_b32_e32 v7, 0xffff0000, v8
	v_lshlrev_b32_e32 v8, 16, v9
	v_and_b32_e32 v9, 0xffff0000, v9
	v_pk_add_f32 v[16:17], v[44:45], v[8:9]
	v_pk_add_f32 v[8:9], v[42:43], v[6:7]
	v_mul_f32_e32 v6, v13, v13
	v_mul_f32_e32 v7, v15, v15
	v_fmac_f32_e32 v6, v12, v12
	v_fmac_f32_e32 v7, v14, v14
	v_add_f32_e32 v6, v6, v7
	v_mul_f32_e32 v7, v9, v9
	v_mul_f32_e32 v18, v17, v17
	v_fmac_f32_e32 v7, v8, v8
	v_fmac_f32_e32 v18, v16, v16
	v_add_f32_e32 v7, v7, v18
	v_add_f32_e32 v18, v6, v7
	v_cvt_pk_bf16_f32 v6, v12, v13
	v_mul_f32_e32 v12, 0x41000000, v12
	v_med3_f32 v19, v12, s64, v250
	v_mul_f32_e32 v12, 0x41000000, v13
	v_med3_f32 v13, v12, s64, v250
	v_mov_b32_e32 v12, v1
	v_cvt_pk_fp8_f32 v12, v19, v13
	v_cvt_pk_bf16_f32 v7, v14, v15
	v_mul_f32_e32 v13, 0x41000000, v14
	v_mul_f32_e32 v14, 0x41000000, v15
	v_med3_f32 v13, v13, s64, v250
	v_med3_f32 v14, v14, s64, v250
	v_cvt_pk_fp8_f32 v12, v13, v14 op_sel:[0,0,1]
	v_mul_f32_e32 v13, 0x41000000, v8
	v_med3_f32 v14, v13, s64, v250
	v_mul_f32_e32 v13, 0x41000000, v9
	v_med3_f32 v15, v13, s64, v250
	v_mov_b32_e32 v13, v1
	v_cvt_pk_fp8_f32 v13, v14, v15
	v_mul_f32_e32 v14, 0x41000000, v16
	v_mul_f32_e32 v15, 0x41000000, v17
	v_med3_f32 v14, v14, s64, v250
	v_med3_f32 v15, v15, s64, v250
	v_cvt_pk_fp8_f32 v13, v14, v15 op_sel:[0,0,1]
	v_lshlrev_b64 v[10:11], 10, v[32:33]
	v_cvt_pk_bf16_f32 v8, v8, v9
	v_cvt_pk_bf16_f32 v9, v16, v17
	v_lshl_add_u64 v[10:11], v[30:31], 0, v[10:11]
	global_store_dwordx4 v[98:99], v[6:9], off
	global_store_dwordx2 v[10:11], v[12:13], off
	v_lshlrev_b32_e32 v6, 16, v2
	v_and_b32_e32 v7, 0xffff0000, v2
	v_lshlrev_b32_e32 v2, 16, v3
	v_and_b32_e32 v3, 0xffff0000, v3
	v_pk_add_f32 v[8:9], v[40:41], v[2:3]
	v_pk_add_f32 v[6:7], v[38:39], v[6:7]
	v_lshlrev_b32_e32 v2, 16, v4
	v_and_b32_e32 v3, 0xffff0000, v4
	v_lshlrev_b32_e32 v4, 16, v5
	v_and_b32_e32 v5, 0xffff0000, v5
	v_pk_add_f32 v[12:13], v[36:37], v[4:5]
	v_pk_add_f32 v[4:5], v[34:35], v[2:3]
	v_mul_f32_e32 v2, v7, v7
	v_mul_f32_e32 v3, v9, v9
	v_fmac_f32_e32 v2, v6, v6
	v_fmac_f32_e32 v3, v8, v8
	v_add_f32_e32 v2, v2, v3
	v_mul_f32_e32 v3, v5, v5
	v_mul_f32_e32 v14, v13, v13
	v_fmac_f32_e32 v3, v4, v4
	v_fmac_f32_e32 v14, v12, v12
	v_add_f32_e32 v3, v3, v14
	v_add_f32_e32 v2, v2, v3
	v_add_f32_e32 v14, v18, v2
	v_cvt_pk_bf16_f32 v2, v6, v7
	v_mul_f32_e32 v6, 0x41000000, v6
	v_med3_f32 v15, v6, s64, v250
	v_mul_f32_e32 v6, 0x41000000, v7
	v_med3_f32 v7, v6, s64, v250
	v_mov_b32_e32 v6, v1
	v_cvt_pk_fp8_f32 v6, v15, v7
	v_cvt_pk_bf16_f32 v3, v8, v9
	v_mul_f32_e32 v7, 0x41000000, v8
	v_mul_f32_e32 v8, 0x41000000, v9
	v_med3_f32 v7, v7, s64, v250
	v_med3_f32 v8, v8, s64, v250
	v_cvt_pk_fp8_f32 v6, v7, v8 op_sel:[0,0,1]
	v_mul_f32_e32 v7, 0x41000000, v4
	v_med3_f32 v8, v7, s64, v250
	v_mul_f32_e32 v7, 0x41000000, v5
	v_med3_f32 v9, v7, s64, v250
	v_mov_b32_e32 v7, v1
	v_cvt_pk_fp8_f32 v7, v8, v9
	v_mul_f32_e32 v8, 0x41000000, v12
	v_mul_f32_e32 v9, 0x41000000, v13
	v_med3_f32 v8, v8, s64, v250
	v_med3_f32 v9, v9, s64, v250
	v_cvt_pk_fp8_f32 v7, v8, v9 op_sel:[0,0,1]
	ds_swizzle_b32 v8, v14 offset:swizzle(SWAP,16)
	v_cvt_pk_bf16_f32 v4, v4, v5
	v_cvt_pk_bf16_f32 v5, v12, v13
	global_store_dwordx4 v[98:99], v[2:5], off offset:256
	global_store_dwordx2 v[10:11], v[6:7], off offset:128
	s_waitcnt lgkmcnt(0)
	v_add_f32_e32 v2, v14, v8
	v_mov_b32_e32 v3, v2
	s_nop 1
	v_permlane32_swap_b32_e32 v2, v3
	s_and_saveexec_b64 s[28:29], s[2:3]
	s_cbranch_execz .LBB0_1877
	v_lshlrev_b64 v[4:5], 6, v[32:33]
	v_lshl_add_u64 v[4:5], s[26:27], 0, v[4:5]
	v_add_f32_e32 v2, v2, v3
	global_store_dword v[4:5], v2, off
